# PART GEMM (Wo,W2) K-loop merged from 8 to 4 barrier-phases per 2 K-tiles; nop-padded section ends
# speedup vs baseline: 1.0039x; 1.0039x over previous
.LBB0_2:
	s_endpgm
	.p2align	8

.LBB1_26:
	v_lshlrev_b32_e32 v0, 4, v141
	s_or_b32 s0, s33, s71
	v_add3_u32 v0, v140, v0, s0
	v_mov_b32_e32 v1, 0
	v_lshlrev_b64 v[8:9], 11, v[0:1]
	v_or_b32_e32 v0, s70, v8
	v_lshl_or_b32 v8, v156, 2, v0
	v_lshlrev_b64 v[60:61], 1, v[8:9]
	v_lshl_add_u64 v[30:31], s[42:43], 0, v[60:61]
	s_movk_i32 s18, 0x2000
	v_add_co_u32_e32 v34, vcc, s18, v30
	s_movk_i32 s17, 0x4000
	s_nop 0
	v_addc_co_u32_e32 v35, vcc, 0, v31, vcc
	s_lshl_b32 s2, s70, 2
	v_add_co_u32_e32 v8, vcc, s17, v30
	s_waitcnt lgkmcnt(0)
	s_add_u32 s0, s44, s2
	v_addc_co_u32_e32 v9, vcc, 0, v31, vcc
	s_movk_i32 s16, 0x6000
	s_addc_u32 s1, s45, 0
	v_add_co_u32_e32 v10, vcc, s16, v30
	v_lshlrev_b32_e32 v38, 4, v156
	s_add_u32 s2, s46, s2
	v_addc_co_u32_e32 v11, vcc, 0, v31, vcc
	s_mov_b32 s15, 0x8000
	s_addc_u32 s3, s47, 0
	global_load_dwordx4 v[0:3], v38, s[0:1]
	global_load_dwordx4 v[4:7], v38, s[2:3]
	global_load_dwordx2 v[42:43], v[8:9], off offset:-4096
	global_load_dwordx2 v[32:33], v[8:9], off
	global_load_dwordx2 v[28:29], v[10:11], off offset:-4096
	global_load_dwordx2 v[26:27], v[10:11], off
	v_add_co_u32_e32 v8, vcc, s15, v30
	s_mov_b32 s14, 0xa000
	s_nop 0
	v_addc_co_u32_e32 v9, vcc, 0, v31, vcc
	v_add_co_u32_e32 v10, vcc, s14, v30
	s_mov_b32 s13, 0xc000
	s_nop 0
	v_addc_co_u32_e32 v11, vcc, 0, v31, vcc
	global_load_dwordx2 v[24:25], v[8:9], off offset:-4096
	global_load_dwordx2 v[22:23], v[8:9], off
	global_load_dwordx2 v[20:21], v[10:11], off offset:-4096
	global_load_dwordx2 v[18:19], v[10:11], off
	v_add_co_u32_e32 v8, vcc, s13, v30
	s_mov_b32 s12, 0xe000
	s_nop 0
	v_addc_co_u32_e32 v9, vcc, 0, v31, vcc
	v_add_co_u32_e32 v36, vcc, s12, v30
	s_mov_b32 s0, 0xf000
	s_nop 0
	v_addc_co_u32_e32 v37, vcc, 0, v31, vcc
	global_load_dwordx2 v[16:17], v[8:9], off offset:-4096
	global_load_dwordx2 v[14:15], v[8:9], off
	global_load_dwordx2 v[12:13], v[36:37], off offset:-4096
	global_load_dwordx2 v[10:11], v[36:37], off
	v_add_co_u32_e32 v36, vcc, s0, v30
	v_lshl_add_u32 v107, v137, 15, 0
	s_nop 0
	v_addc_co_u32_e32 v37, vcc, 0, v31, vcc
	v_lshlrev_b32_e32 v108, 2, v138
	global_load_dwordx2 v[96:97], v[30:31], off
	global_load_dwordx2 v[70:71], v[34:35], off offset:-4096
	global_load_dwordx2 v[68:69], v[34:35], off
	global_load_dwordx2 v[8:9], v[36:37], off
	s_nop 15
	s_nop 15
	s_nop 7
	v_accvgpr_read_b32 v30, a0
	v_accvgpr_read_b32 v31, a1
	v_accvgpr_read_b32 v34, a2
	v_accvgpr_read_b32 v35, a3
	v_accvgpr_read_b32 v36, a4
	v_accvgpr_read_b32 v37, a5
	v_accvgpr_read_b32 v39, a6
	v_accvgpr_read_b32 v40, a7
	v_accvgpr_read_b32 v41, a8
	v_accvgpr_read_b32 v44, a9
	v_accvgpr_read_b32 v45, a10
	v_accvgpr_read_b32 v46, a11
	v_accvgpr_read_b32 v47, a12
	v_accvgpr_read_b32 v48, a13
	v_accvgpr_read_b32 v49, a14
	v_accvgpr_read_b32 v50, a15
	v_add3_u32 v107, v107, v139, v108
	v_accvgpr_read_b32 v51, a16
	v_accvgpr_read_b32 v52, a17
	v_accvgpr_read_b32 v53, a18
	v_accvgpr_read_b32 v54, a19
	v_accvgpr_read_b32 v55, a20
	v_accvgpr_read_b32 v56, a21
	v_accvgpr_read_b32 v57, a22
	v_accvgpr_read_b32 v58, a23
	v_accvgpr_read_b32 v59, a24
	v_accvgpr_read_b32 v62, a25
	v_accvgpr_read_b32 v63, a26
	v_accvgpr_read_b32 v64, a27
	v_accvgpr_read_b32 v65, a28
	v_accvgpr_read_b32 v66, a29
	v_accvgpr_read_b32 v67, a30
	v_accvgpr_read_b32 v72, a31
	s_mov_b32 s28, 0x3727c5ac
	v_accvgpr_read_b32 v73, a32
	v_accvgpr_read_b32 v74, a33
	v_accvgpr_read_b32 v75, a34
	v_accvgpr_read_b32 v76, a35
	v_accvgpr_read_b32 v77, a36
	v_accvgpr_read_b32 v78, a37
	v_accvgpr_read_b32 v79, a38
	v_accvgpr_read_b32 v80, a39
	v_accvgpr_read_b32 v81, a40
	v_accvgpr_read_b32 v82, a41
	v_accvgpr_read_b32 v83, a42
	v_accvgpr_read_b32 v84, a43
	v_accvgpr_read_b32 v85, a44
	v_accvgpr_read_b32 v86, a45
	v_accvgpr_read_b32 v87, a46
	v_accvgpr_read_b32 v88, a47
	v_lshl_add_u64 v[60:61], s[48:49], 0, v[60:61]
	v_accvgpr_read_b32 v89, a48
	v_accvgpr_read_b32 v90, a49
	v_accvgpr_read_b32 v91, a50
	v_accvgpr_read_b32 v92, a51
	v_accvgpr_read_b32 v93, a52
	v_accvgpr_read_b32 v94, a53
	v_accvgpr_read_b32 v95, a54
	v_accvgpr_read_b32 v98, a55
	v_accvgpr_read_b32 v99, a56
	v_accvgpr_read_b32 v100, a57
	v_accvgpr_read_b32 v101, a58
	v_accvgpr_read_b32 v102, a59
	v_accvgpr_read_b32 v103, a60
	v_accvgpr_read_b32 v104, a61
	v_accvgpr_read_b32 v105, a62
	v_accvgpr_read_b32 v106, a63
	s_nop 0
	v_accvgpr_read_b32 v108, a64
	v_accvgpr_read_b32 v109, a65
	v_accvgpr_read_b32 v110, a66
	v_accvgpr_read_b32 v111, a67
	v_accvgpr_read_b32 v112, a68
	v_accvgpr_read_b32 v113, a69
	v_accvgpr_read_b32 v114, a70
	v_accvgpr_read_b32 v115, a71
	v_accvgpr_read_b32 v116, a72
	v_accvgpr_read_b32 v117, a73
	v_accvgpr_read_b32 v118, a74
	v_accvgpr_read_b32 v119, a75
	v_accvgpr_read_b32 v120, a76
	v_accvgpr_read_b32 v121, a77
	v_accvgpr_read_b32 v122, a78
	v_accvgpr_read_b32 v123, a79
	s_nop 0
	v_accvgpr_read_b32 v124, a80
	v_accvgpr_read_b32 v125, a81
	v_accvgpr_read_b32 v126, a82
	v_accvgpr_read_b32 v127, a83
	v_accvgpr_read_b32 v128, a84
	v_accvgpr_read_b32 v129, a85
	v_accvgpr_read_b32 v130, a86
	v_accvgpr_read_b32 v131, a87
	v_accvgpr_read_b32 v132, a88
	v_accvgpr_read_b32 v133, a89
	v_accvgpr_read_b32 v134, a90
	v_accvgpr_read_b32 v135, a91
	v_accvgpr_read_b32 v137, a92
	v_accvgpr_read_b32 v138, a93
	v_accvgpr_read_b32 v139, a94
	v_accvgpr_read_b32 v140, a95
	s_nop 0
	v_accvgpr_read_b32 v141, a96
	v_accvgpr_read_b32 v142, a97
	v_accvgpr_read_b32 v144, a98
	v_accvgpr_read_b32 v145, a99
	v_accvgpr_read_b32 v146, a100
	v_accvgpr_read_b32 v147, a101
	v_accvgpr_read_b32 v148, a102
	v_accvgpr_read_b32 v149, a103
	v_accvgpr_read_b32 v150, a104
	v_accvgpr_read_b32 v151, a105
	v_accvgpr_read_b32 v152, a106
	v_accvgpr_read_b32 v153, a107
	v_accvgpr_read_b32 v154, a108
	v_accvgpr_read_b32 v155, a109
	v_accvgpr_read_b32 v156, a110
	v_accvgpr_read_b32 v157, a111
	s_nop 0
	v_accvgpr_read_b32 v158, a112
	v_accvgpr_read_b32 v159, a113
	v_accvgpr_read_b32 v160, a114
	v_accvgpr_read_b32 v161, a115
	v_accvgpr_read_b32 v162, a116
	v_accvgpr_read_b32 v163, a117
	v_accvgpr_read_b32 v164, a118
	v_accvgpr_read_b32 v165, a119
	v_accvgpr_read_b32 v166, a120
	v_accvgpr_read_b32 v167, a121
	v_accvgpr_read_b32 v168, a122
	v_accvgpr_read_b32 v169, a123
	v_accvgpr_read_b32 v170, a124
	v_accvgpr_read_b32 v171, a125
	v_accvgpr_read_b32 v172, a126
	v_accvgpr_read_b32 v173, a127
	s_waitcnt vmcnt(0)
	s_barrier
	ds_write2_b32 v107, v30, v51 offset1:32
	v_add_u32_e32 v30, 0x400, v107
	ds_write2_b32 v30, v31, v52 offset1:32
	v_add_u32_e32 v31, 0x800, v107
	ds_write2_b32 v31, v34, v53 offset1:32
	v_add_u32_e32 v34, 0xc00, v107
	ds_write2_b32 v34, v35, v54 offset1:32
	v_add_u32_e32 v35, 0x2000, v107
	ds_write2_b32 v35, v36, v55 offset1:32
	v_add_u32_e32 v36, 0x2400, v107
	ds_write2_b32 v36, v37, v56 offset1:32
	v_add_u32_e32 v37, 0x2800, v107
	ds_write2_b32 v37, v39, v57 offset1:32
	v_add_u32_e32 v39, 0x2c00, v107
	ds_write2_b32 v39, v40, v58 offset1:32
	v_add_u32_e32 v40, 0x4000, v107
	ds_write2_b32 v40, v41, v59 offset1:32
	v_add_u32_e32 v41, 0x4400, v107
	ds_write2_b32 v41, v44, v62 offset1:32
	v_add_u32_e32 v44, 0x4800, v107
	ds_write2_b32 v44, v45, v63 offset1:32
	v_add_u32_e32 v45, 0x4c00, v107
	ds_write2_b32 v45, v46, v64 offset1:32
	v_add_u32_e32 v46, 0x6000, v107
	ds_write2_b32 v46, v47, v65 offset1:32
	v_add_u32_e32 v47, 0x6400, v107
	ds_write2_b32 v47, v48, v66 offset1:32
	v_add_u32_e32 v48, 0x6800, v107
	ds_write2_b32 v48, v49, v67 offset1:32
	v_add_u32_e32 v49, 0x6c00, v107
	ds_write2_b32 v49, v50, v72 offset1:32
	ds_write2_b32 v107, v73, v89 offset0:64 offset1:96
	ds_write2_b32 v30, v74, v90 offset0:64 offset1:96
	ds_write2_b32 v31, v75, v91 offset0:64 offset1:96
	ds_write2_b32 v34, v76, v92 offset0:64 offset1:96
	ds_write2_b32 v35, v77, v93 offset0:64 offset1:96
	ds_write2_b32 v36, v78, v94 offset0:64 offset1:96
	ds_write2_b32 v37, v79, v95 offset0:64 offset1:96
	ds_write2_b32 v39, v80, v98 offset0:64 offset1:96
	ds_write2_b32 v40, v81, v99 offset0:64 offset1:96
	ds_write2_b32 v41, v82, v100 offset0:64 offset1:96
	ds_write2_b32 v44, v83, v101 offset0:64 offset1:96
	ds_write2_b32 v45, v84, v102 offset0:64 offset1:96
	ds_write2_b32 v46, v85, v103 offset0:64 offset1:96
	ds_write2_b32 v47, v86, v104 offset0:64 offset1:96
	ds_write2_b32 v48, v87, v105 offset0:64 offset1:96
	ds_write2_b32 v49, v88, v106 offset0:64 offset1:96
	ds_write2_b32 v107, v108, v124 offset0:128 offset1:160
	ds_write2_b32 v30, v109, v125 offset0:128 offset1:160
	ds_write2_b32 v31, v110, v126 offset0:128 offset1:160
	ds_write2_b32 v34, v111, v127 offset0:128 offset1:160
	ds_write2_b32 v35, v112, v128 offset0:128 offset1:160
	ds_write2_b32 v36, v113, v129 offset0:128 offset1:160
	ds_write2_b32 v37, v114, v130 offset0:128 offset1:160
	ds_write2_b32 v39, v115, v131 offset0:128 offset1:160
	ds_write2_b32 v40, v116, v132 offset0:128 offset1:160
	ds_write2_b32 v41, v117, v133 offset0:128 offset1:160
	ds_write2_b32 v44, v118, v134 offset0:128 offset1:160
	ds_write2_b32 v45, v119, v135 offset0:128 offset1:160
	ds_write2_b32 v46, v120, v137 offset0:128 offset1:160
	ds_write2_b32 v47, v121, v138 offset0:128 offset1:160
	ds_write2_b32 v48, v122, v139 offset0:128 offset1:160
	ds_write2_b32 v49, v123, v140 offset0:128 offset1:160
	ds_write2_b32 v107, v141, v158 offset0:192 offset1:224
	ds_write2_b32 v30, v142, v159 offset0:192 offset1:224
	ds_write2_b32 v31, v144, v160 offset0:192 offset1:224
	ds_write2_b32 v34, v145, v161 offset0:192 offset1:224
	ds_write2_b32 v35, v146, v162 offset0:192 offset1:224
	ds_write2_b32 v36, v147, v163 offset0:192 offset1:224
	ds_write2_b32 v37, v148, v164 offset0:192 offset1:224
	ds_write2_b32 v39, v149, v165 offset0:192 offset1:224
	ds_write2_b32 v40, v150, v166 offset0:192 offset1:224
	ds_write2_b32 v41, v151, v167 offset0:192 offset1:224
	ds_write2_b32 v44, v152, v168 offset0:192 offset1:224
	ds_write2_b32 v45, v153, v169 offset0:192 offset1:224
	ds_write2_b32 v46, v154, v170 offset0:192 offset1:224
	ds_write2_b32 v47, v155, v171 offset0:192 offset1:224
	ds_write2_b32 v48, v156, v172 offset0:192 offset1:224
	ds_write2_b32 v49, v157, v173 offset0:192 offset1:224
	v_lshl_add_u32 v30, v136, 15, 0
	v_add3_u32 v116, v30, v143, v38
	v_add_u32_e32 v30, 0x10000, v116
	s_waitcnt lgkmcnt(0)
	s_barrier
	ds_read_b128 v[34:37], v30
	ds_read_b128 v[38:41], v116
	ds_read_b128 v[44:47], v116 offset:1024
	v_add_u32_e32 v30, 0x10400, v116
	ds_read_b128 v[48:51], v30
	s_waitcnt lgkmcnt(2)
	v_pk_add_f32 v[102:103], v[40:41], v[36:37]
	v_pk_add_f32 v[104:105], v[38:39], v[34:35]
	v_add_u32_e32 v38, 0x10800, v116
	v_mov_b32_e32 v34, v104
	v_mov_b32_e32 v35, v103
	ds_read_b128 v[38:41], v38
	v_pk_mov_b32 v[30:31], v[104:105], v[102:103] op_sel:[1,0]
	s_waitcnt lgkmcnt(1)
	v_pk_add_f32 v[98:99], v[46:47], v[50:51]
	v_pk_add_f32 v[132:133], v[30:31], v[34:35]
	v_pk_add_f32 v[100:101], v[44:45], v[48:49]
	ds_read_b128 v[34:37], v116 offset:2048
	v_pk_mov_b32 v[30:31], v[100:101], v[98:99] op_sel:[1,0]
	v_mov_b32_e32 v44, v100
	v_mov_b32_e32 v45, v99
	v_pk_add_f32 v[122:123], v[30:31], v[44:45]
	v_add_u32_e32 v30, 0x10c00, v116
	ds_read_b128 v[44:47], v116 offset:3072
	ds_read_b128 v[48:51], v30
	s_waitcnt lgkmcnt(2)
	v_pk_add_f32 v[92:93], v[36:37], v[40:41]
	v_pk_add_f32 v[94:95], v[34:35], v[38:39]
	v_mov_b32_e32 v35, v93
	v_pk_mov_b32 v[30:31], v[94:95], v[92:93] op_sel:[1,0]
	v_mov_b32_e32 v34, v94
	v_pk_add_f32 v[118:119], v[30:31], v[34:35]
	v_add_u32_e32 v34, 0x11000, v116
	s_waitcnt lgkmcnt(0)
	v_pk_add_f32 v[88:89], v[46:47], v[50:51]
	v_pk_add_f32 v[90:91], v[44:45], v[48:49]
	ds_read_b128 v[34:37], v34
	ds_read_b128 v[38:41], v116 offset:4096
	ds_read_b128 v[44:47], v116 offset:5120
	v_pk_mov_b32 v[30:31], v[90:91], v[88:89] op_sel:[1,0]
	v_mov_b32_e32 v52, v90
	v_add_u32_e32 v48, 0x11400, v116
	v_mov_b32_e32 v53, v89
	ds_read_b128 v[48:51], v48
	v_pk_add_f32 v[120:121], v[30:31], v[52:53]
	v_add_u32_e32 v30, 0x11800, v116
	s_waitcnt lgkmcnt(2)
	v_pk_add_f32 v[84:85], v[40:41], v[36:37]
	v_pk_add_f32 v[86:87], v[38:39], v[34:35]
	ds_read_b128 v[34:37], v116 offset:6144
	ds_read_b128 v[38:41], v30
	v_add_u32_e32 v30, 0x11c00, v116
	s_waitcnt lgkmcnt(2)
	v_pk_add_f32 v[80:81], v[46:47], v[50:51]
	v_pk_add_f32 v[82:83], v[44:45], v[48:49]
	ds_read_b128 v[48:51], v30
	v_add_u32_e32 v30, 0x12000, v116
	ds_read_b128 v[44:47], v116 offset:7168
	s_waitcnt lgkmcnt(2)
	v_pk_add_f32 v[74:75], v[36:37], v[40:41]
	v_pk_add_f32 v[76:77], v[34:35], v[38:39]
	ds_read_b128 v[34:37], v30
	ds_read_b128 v[38:41], v116 offset:8192
	ds_read_b128 v[52:55], v116 offset:9216
	v_add_u32_e32 v30, 0x12400, v116
	ds_read_b128 v[56:59], v30
	s_waitcnt lgkmcnt(4)
	v_pk_add_f32 v[72:73], v[46:47], v[50:51]
	s_waitcnt lgkmcnt(2)
	v_pk_add_f32 v[64:65], v[40:41], v[36:37]
	v_pk_add_f32 v[66:67], v[38:39], v[34:35]
	ds_read_b128 v[34:37], v116 offset:10240
	v_add_u32_e32 v30, 0x12800, v116
	ds_read_b128 v[38:41], v30
	v_pk_add_f32 v[78:79], v[44:45], v[48:49]
	ds_read_b128 v[44:47], v116 offset:11264
	v_add_u32_e32 v30, 0x12c00, v116
	ds_read_b128 v[48:51], v30
	v_add_u32_e32 v30, 0x13000, v116
	s_waitcnt lgkmcnt(4)
	v_pk_add_f32 v[58:59], v[54:55], v[58:59]
	v_pk_add_f32 v[62:63], v[52:53], v[56:57]
	s_waitcnt lgkmcnt(2)
	v_pk_add_f32 v[52:53], v[36:37], v[40:41]
	v_pk_add_f32 v[54:55], v[34:35], v[38:39]
	ds_read_b128 v[34:37], v30
	ds_read_b128 v[38:41], v116 offset:12288
	ds_read_b128 v[106:109], v116 offset:13312
	v_add_u32_e32 v30, 0x13400, v116
	ds_read_b128 v[110:113], v30
	s_waitcnt lgkmcnt(4)
	v_pk_add_f32 v[50:51], v[46:47], v[50:51]
	v_pk_add_f32 v[56:57], v[44:45], v[48:49]
	s_waitcnt lgkmcnt(2)
	v_pk_add_f32 v[46:47], v[40:41], v[36:37]
	v_pk_add_f32 v[48:49], v[38:39], v[34:35]
	ds_read_b128 v[34:37], v116 offset:14336
	v_add_u32_e32 v30, 0x13800, v116
	s_waitcnt lgkmcnt(1)
	v_pk_add_f32 v[40:41], v[108:109], v[112:113]
	ds_read_b128 v[112:115], v30
	v_pk_add_f32 v[44:45], v[106:107], v[110:111]
	ds_read_b128 v[106:109], v116 offset:15360
	v_add_u32_e32 v30, 0x13c00, v116
	ds_read_b128 v[124:127], v30
	s_waitcnt lgkmcnt(2)
	v_pk_add_f32 v[38:39], v[34:35], v[112:113]
	v_pk_mov_b32 v[30:31], v[86:87], v[84:85] op_sel:[1,0]
	v_mov_b32_e32 v34, v86
	v_mov_b32_e32 v35, v85
	v_pk_add_f32 v[136:137], v[30:31], v[34:35]
	v_pk_mov_b32 v[30:31], v[82:83], v[80:81] op_sel:[1,0]
	v_mov_b32_e32 v34, v82
	v_mov_b32_e32 v35, v81
	v_pk_add_f32 v[134:135], v[30:31], v[34:35]
	s_waitcnt lgkmcnt(0)
	v_pk_add_f32 v[30:31], v[108:109], v[126:127]
	v_pk_add_f32 v[34:35], v[106:107], v[124:125]
	v_pk_mov_b32 v[106:107], v[76:77], v[74:75] op_sel:[1,0]
	v_mov_b32_e32 v108, v76
	v_mov_b32_e32 v109, v75
	v_add_f32_e32 v132, v132, v133
	v_pk_add_f32 v[130:131], v[106:107], v[108:109]
	v_pk_mov_b32 v[106:107], v[78:79], v[72:73] op_sel:[1,0]
	v_mov_b32_e32 v108, v78
	v_mov_b32_e32 v109, v73
	v_add_f32_dpp v132, v132, v132 quad_perm:[1,0,3,2] row_mask:0xf bank_mask:0xf bound_ctrl:1
	v_pk_add_f32 v[128:129], v[106:107], v[108:109]
	v_mov_b32_e32 v106, v66
	v_mov_b32_e32 v107, v65
	v_pk_mov_b32 v[108:109], v[66:67], v[64:65] op_sel:[1,0]
	v_add_f32_dpp v132, v132, v132 quad_perm:[2,3,0,1] row_mask:0xf bank_mask:0xf bound_ctrl:1
	v_add_f32_e32 v122, v122, v123
	v_pk_add_f32 v[126:127], v[108:109], v[106:107]
	v_mov_b32_e32 v106, v62
	v_mov_b32_e32 v107, v59
	v_pk_mov_b32 v[108:109], v[62:63], v[58:59] op_sel:[1,0]
	v_add_f32_dpp v132, v132, v132 row_half_mirror row_mask:0xf bank_mask:0xf bound_ctrl:1
	v_add_f32_dpp v122, v122, v122 quad_perm:[1,0,3,2] row_mask:0xf bank_mask:0xf bound_ctrl:1
	v_pk_add_f32 v[124:125], v[108:109], v[106:107]
	v_mov_b32_e32 v106, v54
	v_mov_b32_e32 v107, v53
	v_pk_mov_b32 v[108:109], v[54:55], v[52:53] op_sel:[1,0]
	v_add_f32_dpp v132, v132, v132 row_mirror row_mask:0xf bank_mask:0xf bound_ctrl:1
	v_add_f32_dpp v122, v122, v122 quad_perm:[2,3,0,1] row_mask:0xf bank_mask:0xf bound_ctrl:1
	v_add_f32_e32 v118, v118, v119
	v_pk_add_f32 v[116:117], v[108:109], v[106:107]
	v_mov_b32_e32 v106, v56
	v_mov_b32_e32 v107, v51
	v_pk_mov_b32 v[108:109], v[56:57], v[50:51] op_sel:[1,0]
	v_readlane_b32 s2, v132, 16
	v_readlane_b32 s3, v132, 48
	v_add_f32_dpp v122, v122, v122 row_half_mirror row_mask:0xf bank_mask:0xf bound_ctrl:1
	v_add_f32_dpp v118, v118, v118 quad_perm:[1,0,3,2] row_mask:0xf bank_mask:0xf bound_ctrl:1
	v_pk_add_f32 v[36:37], v[36:37], v[114:115]
	v_pk_add_f32 v[114:115], v[108:109], v[106:107]
	v_mov_b32_e32 v106, v48
	v_mov_b32_e32 v107, v47
	v_pk_mov_b32 v[108:109], v[48:49], v[46:47] op_sel:[1,0]
	v_readlane_b32 s0, v132, 0
	v_readlane_b32 s1, v132, 32
	v_mov_b32_e32 v132, s2
	v_mov_b32_e32 v133, s3
	v_add_f32_dpp v122, v122, v122 row_mirror row_mask:0xf bank_mask:0xf bound_ctrl:1
	v_add_f32_dpp v118, v118, v118 quad_perm:[2,3,0,1] row_mask:0xf bank_mask:0xf bound_ctrl:1
	v_add_f32_e32 v120, v120, v121
	v_pk_add_f32 v[112:113], v[108:109], v[106:107]
	v_mov_b32_e32 v106, v44
	v_mov_b32_e32 v107, v41
	v_pk_mov_b32 v[108:109], v[44:45], v[40:41] op_sel:[1,0]
	v_pk_add_f32 v[132:133], s[0:1], v[132:133]
	v_readlane_b32 s2, v122, 16
	v_readlane_b32 s3, v122, 48
	v_add_f32_dpp v118, v118, v118 row_half_mirror row_mask:0xf bank_mask:0xf bound_ctrl:1
	v_add_f32_dpp v120, v120, v120 quad_perm:[1,0,3,2] row_mask:0xf bank_mask:0xf bound_ctrl:1
	v_pk_add_f32 v[110:111], v[108:109], v[106:107]
	v_mov_b32_e32 v106, v38
	v_mov_b32_e32 v107, v37
	v_pk_mov_b32 v[108:109], v[38:39], v[36:37] op_sel:[1,0]
	v_add_f32_e32 v132, v132, v133
	v_readlane_b32 s0, v122, 0
	v_readlane_b32 s1, v122, 32
	v_mov_b32_e32 v122, s2
	v_mov_b32_e32 v123, s3
	v_add_f32_dpp v118, v118, v118 row_mirror row_mask:0xf bank_mask:0xf bound_ctrl:1
	v_add_f32_dpp v120, v120, v120 quad_perm:[2,3,0,1] row_mask:0xf bank_mask:0xf bound_ctrl:1
	v_add_f32_e32 v136, v136, v137
	v_pk_add_f32 v[108:109], v[108:109], v[106:107]
	v_mov_b32_e32 v106, v34
	v_mov_b32_e32 v107, v31
	v_pk_mov_b32 v[138:139], v[34:35], v[30:31] op_sel:[1,0]
	v_fmamk_f32 v105, v132, 0xbb800000, v105
	v_fmac_f32_e32 v104, 0xbb800000, v132
	v_fmamk_f32 v103, v132, 0xbb800000, v103
	v_fmac_f32_e32 v102, 0xbb800000, v132
	v_pk_add_f32 v[122:123], s[0:1], v[122:123]
	v_readlane_b32 s2, v118, 16
	v_readlane_b32 s3, v118, 48
	v_add_f32_dpp v120, v120, v120 row_half_mirror row_mask:0xf bank_mask:0xf bound_ctrl:1
	v_add_f32_dpp v136, v136, v136 quad_perm:[1,0,3,2] row_mask:0xf bank_mask:0xf bound_ctrl:1
	v_pk_add_f32 v[106:107], v[138:139], v[106:107]
	v_pk_mul_f32 v[132:133], v[102:103], v[102:103]
	v_pk_mul_f32 v[138:139], v[104:105], v[104:105]
	v_add_f32_e32 v122, v122, v123
	v_readlane_b32 s0, v118, 0
	v_readlane_b32 s1, v118, 32
	v_mov_b32_e32 v118, s2
	v_mov_b32_e32 v119, s3
	v_add_f32_dpp v120, v120, v120 row_mirror row_mask:0xf bank_mask:0xf bound_ctrl:1
	v_add_f32_dpp v136, v136, v136 quad_perm:[2,3,0,1] row_mask:0xf bank_mask:0xf bound_ctrl:1
	v_add_f32_e32 v134, v134, v135
	v_pk_mov_b32 v[140:141], v[138:139], v[132:133] op_sel:[1,0]
	v_mov_b32_e32 v139, v133
	v_fmamk_f32 v101, v122, 0xbb800000, v101
	v_fmac_f32_e32 v100, 0xbb800000, v122
	v_fmamk_f32 v99, v122, 0xbb800000, v99
	v_fmac_f32_e32 v98, 0xbb800000, v122
	v_pk_add_f32 v[118:119], s[0:1], v[118:119]
	v_readlane_b32 s2, v120, 16
	v_readlane_b32 s3, v120, 48
	v_add_f32_dpp v136, v136, v136 row_half_mirror row_mask:0xf bank_mask:0xf bound_ctrl:1
	v_add_f32_dpp v134, v134, v134 quad_perm:[1,0,3,2] row_mask:0xf bank_mask:0xf bound_ctrl:1
	v_pk_add_f32 v[132:133], v[140:141], v[138:139]
	v_pk_mul_f32 v[122:123], v[98:99], v[98:99]
	v_pk_mul_f32 v[138:139], v[100:101], v[100:101]
	v_add_f32_e32 v118, v118, v119
	v_readlane_b32 s0, v120, 0
	v_readlane_b32 s1, v120, 32
	v_mov_b32_e32 v120, s2
	v_mov_b32_e32 v121, s3
	v_add_f32_dpp v136, v136, v136 row_mirror row_mask:0xf bank_mask:0xf bound_ctrl:1
	v_add_f32_dpp v134, v134, v134 quad_perm:[2,3,0,1] row_mask:0xf bank_mask:0xf bound_ctrl:1
	v_add_f32_e32 v130, v130, v131
	v_pk_mov_b32 v[140:141], v[138:139], v[122:123] op_sel:[1,0]
	v_mov_b32_e32 v139, v123
	v_fmamk_f32 v95, v118, 0xbb800000, v95
	v_fmac_f32_e32 v94, 0xbb800000, v118
	v_fmamk_f32 v93, v118, 0xbb800000, v93
	v_fmac_f32_e32 v92, 0xbb800000, v118
	v_pk_add_f32 v[120:121], s[0:1], v[120:121]
	v_readlane_b32 s2, v136, 16
	v_readlane_b32 s3, v136, 48
	v_add_f32_dpp v134, v134, v134 row_half_mirror row_mask:0xf bank_mask:0xf bound_ctrl:1
	v_add_f32_dpp v130, v130, v130 quad_perm:[1,0,3,2] row_mask:0xf bank_mask:0xf bound_ctrl:1
	v_pk_add_f32 v[122:123], v[140:141], v[138:139]
	v_pk_mul_f32 v[118:119], v[92:93], v[92:93]
	v_pk_mul_f32 v[138:139], v[94:95], v[94:95]
	v_add_f32_e32 v120, v120, v121
	v_readlane_b32 s0, v136, 0
	v_readlane_b32 s1, v136, 32
	v_mov_b32_e32 v136, s2
	v_mov_b32_e32 v137, s3
	v_add_f32_dpp v134, v134, v134 row_mirror row_mask:0xf bank_mask:0xf bound_ctrl:1
	v_add_f32_dpp v130, v130, v130 quad_perm:[2,3,0,1] row_mask:0xf bank_mask:0xf bound_ctrl:1
	v_add_f32_e32 v128, v128, v129
	v_pk_mov_b32 v[140:141], v[138:139], v[118:119] op_sel:[1,0]
	v_mov_b32_e32 v139, v119
	v_fmamk_f32 v91, v120, 0xbb800000, v91
	v_fmac_f32_e32 v90, 0xbb800000, v120
	v_fmamk_f32 v89, v120, 0xbb800000, v89
	v_fmac_f32_e32 v88, 0xbb800000, v120
	v_pk_add_f32 v[136:137], s[0:1], v[136:137]
	v_readlane_b32 s2, v134, 16
	v_readlane_b32 s3, v134, 48
	v_add_f32_dpp v130, v130, v130 row_half_mirror row_mask:0xf bank_mask:0xf bound_ctrl:1
	v_add_f32_dpp v128, v128, v128 quad_perm:[1,0,3,2] row_mask:0xf bank_mask:0xf bound_ctrl:1
	v_pk_add_f32 v[118:119], v[140:141], v[138:139]
	v_pk_mul_f32 v[120:121], v[88:89], v[88:89]
	v_pk_mul_f32 v[138:139], v[90:91], v[90:91]
	v_add_f32_e32 v136, v136, v137
	v_readlane_b32 s0, v134, 0
	v_readlane_b32 s1, v134, 32
	v_mov_b32_e32 v134, s2
	v_mov_b32_e32 v135, s3
	v_add_f32_dpp v130, v130, v130 row_mirror row_mask:0xf bank_mask:0xf bound_ctrl:1
	v_add_f32_dpp v128, v128, v128 quad_perm:[2,3,0,1] row_mask:0xf bank_mask:0xf bound_ctrl:1
	v_add_f32_e32 v126, v126, v127
	v_pk_mov_b32 v[140:141], v[138:139], v[120:121] op_sel:[1,0]
	v_mov_b32_e32 v139, v121
	v_fmamk_f32 v87, v136, 0xbb800000, v87
	v_fmac_f32_e32 v86, 0xbb800000, v136
	v_fmamk_f32 v85, v136, 0xbb800000, v85
	v_fmac_f32_e32 v84, 0xbb800000, v136
	v_pk_add_f32 v[134:135], s[0:1], v[134:135]
	v_readlane_b32 s2, v130, 16
	v_readlane_b32 s3, v130, 48
	v_add_f32_dpp v128, v128, v128 row_half_mirror row_mask:0xf bank_mask:0xf bound_ctrl:1
	v_add_f32_dpp v126, v126, v126 quad_perm:[1,0,3,2] row_mask:0xf bank_mask:0xf bound_ctrl:1
	v_pk_add_f32 v[120:121], v[140:141], v[138:139]
	v_pk_mul_f32 v[136:137], v[84:85], v[84:85]
	v_pk_mul_f32 v[138:139], v[86:87], v[86:87]
	v_add_f32_e32 v134, v134, v135
	v_readlane_b32 s0, v130, 0
	v_readlane_b32 s1, v130, 32
	v_mov_b32_e32 v130, s2
	v_mov_b32_e32 v131, s3
	v_add_f32_dpp v128, v128, v128 row_mirror row_mask:0xf bank_mask:0xf bound_ctrl:1
	v_add_f32_dpp v126, v126, v126 quad_perm:[2,3,0,1] row_mask:0xf bank_mask:0xf bound_ctrl:1
	v_add_f32_e32 v124, v124, v125
	v_pk_mov_b32 v[140:141], v[138:139], v[136:137] op_sel:[1,0]
	v_mov_b32_e32 v139, v137
	v_fmamk_f32 v83, v134, 0xbb800000, v83
	v_fmac_f32_e32 v82, 0xbb800000, v134
	v_fmamk_f32 v81, v134, 0xbb800000, v81
	v_fmac_f32_e32 v80, 0xbb800000, v134
	v_pk_add_f32 v[130:131], s[0:1], v[130:131]
	v_readlane_b32 s2, v128, 16
	v_readlane_b32 s3, v128, 48
	v_add_f32_dpp v126, v126, v126 row_half_mirror row_mask:0xf bank_mask:0xf bound_ctrl:1
	v_add_f32_dpp v124, v124, v124 quad_perm:[1,0,3,2] row_mask:0xf bank_mask:0xf bound_ctrl:1
	v_pk_add_f32 v[136:137], v[140:141], v[138:139]
	v_pk_mul_f32 v[134:135], v[80:81], v[80:81]
	v_pk_mul_f32 v[138:139], v[82:83], v[82:83]
	v_add_f32_e32 v130, v130, v131
	v_readlane_b32 s0, v128, 0
	v_readlane_b32 s1, v128, 32
	v_mov_b32_e32 v128, s2
	v_mov_b32_e32 v129, s3
	v_add_f32_dpp v126, v126, v126 row_mirror row_mask:0xf bank_mask:0xf bound_ctrl:1
	v_add_f32_dpp v124, v124, v124 quad_perm:[2,3,0,1] row_mask:0xf bank_mask:0xf bound_ctrl:1
	v_add_f32_e32 v116, v116, v117
	v_pk_mov_b32 v[140:141], v[138:139], v[134:135] op_sel:[1,0]
	v_mov_b32_e32 v139, v135
	v_fmamk_f32 v77, v130, 0xbb800000, v77
	v_fmac_f32_e32 v76, 0xbb800000, v130
	v_fmamk_f32 v75, v130, 0xbb800000, v75
	v_fmac_f32_e32 v74, 0xbb800000, v130
	v_pk_add_f32 v[128:129], s[0:1], v[128:129]
	v_readlane_b32 s2, v126, 16
	v_readlane_b32 s3, v126, 48
	v_add_f32_dpp v124, v124, v124 row_half_mirror row_mask:0xf bank_mask:0xf bound_ctrl:1
	v_add_f32_dpp v116, v116, v116 quad_perm:[1,0,3,2] row_mask:0xf bank_mask:0xf bound_ctrl:1
	v_pk_add_f32 v[134:135], v[140:141], v[138:139]
	v_pk_mul_f32 v[130:131], v[74:75], v[74:75]
	v_pk_mul_f32 v[138:139], v[76:77], v[76:77]
	v_add_f32_e32 v128, v128, v129
	v_readlane_b32 s0, v126, 0
	v_readlane_b32 s1, v126, 32
	v_mov_b32_e32 v126, s2
	v_mov_b32_e32 v127, s3
	v_add_f32_dpp v124, v124, v124 row_mirror row_mask:0xf bank_mask:0xf bound_ctrl:1
	v_add_f32_dpp v116, v116, v116 quad_perm:[2,3,0,1] row_mask:0xf bank_mask:0xf bound_ctrl:1
	v_add_f32_e32 v114, v114, v115
	v_pk_mov_b32 v[140:141], v[138:139], v[130:131] op_sel:[1,0]
	v_mov_b32_e32 v139, v131
	v_fmamk_f32 v79, v128, 0xbb800000, v79
	v_fmac_f32_e32 v78, 0xbb800000, v128
	v_fmamk_f32 v73, v128, 0xbb800000, v73
	v_fmac_f32_e32 v72, 0xbb800000, v128
	v_pk_add_f32 v[126:127], s[0:1], v[126:127]
	v_readlane_b32 s2, v124, 16
	v_readlane_b32 s3, v124, 48
	v_add_f32_dpp v116, v116, v116 row_half_mirror row_mask:0xf bank_mask:0xf bound_ctrl:1
	v_add_f32_dpp v114, v114, v114 quad_perm:[1,0,3,2] row_mask:0xf bank_mask:0xf bound_ctrl:1
	v_pk_add_f32 v[130:131], v[140:141], v[138:139]
	v_pk_mul_f32 v[128:129], v[72:73], v[72:73]
	v_pk_mul_f32 v[138:139], v[78:79], v[78:79]
	v_add_f32_e32 v126, v126, v127
	v_readlane_b32 s0, v124, 0
	v_readlane_b32 s1, v124, 32
	v_mov_b32_e32 v124, s2
	v_mov_b32_e32 v125, s3
	v_add_f32_dpp v116, v116, v116 row_mirror row_mask:0xf bank_mask:0xf bound_ctrl:1
	v_add_f32_dpp v114, v114, v114 quad_perm:[2,3,0,1] row_mask:0xf bank_mask:0xf bound_ctrl:1
	v_add_f32_e32 v112, v112, v113
	v_pk_mov_b32 v[140:141], v[138:139], v[128:129] op_sel:[1,0]
	v_mov_b32_e32 v139, v129
	v_fmamk_f32 v67, v126, 0xbb800000, v67
	v_fmac_f32_e32 v66, 0xbb800000, v126
	v_fmamk_f32 v65, v126, 0xbb800000, v65
	v_fmac_f32_e32 v64, 0xbb800000, v126
	v_pk_add_f32 v[124:125], s[0:1], v[124:125]
	v_readlane_b32 s2, v116, 16
	v_readlane_b32 s3, v116, 48
	v_add_f32_dpp v114, v114, v114 row_half_mirror row_mask:0xf bank_mask:0xf bound_ctrl:1
	v_add_f32_dpp v112, v112, v112 quad_perm:[1,0,3,2] row_mask:0xf bank_mask:0xf bound_ctrl:1
	v_pk_add_f32 v[128:129], v[140:141], v[138:139]
	v_pk_mul_f32 v[126:127], v[64:65], v[64:65]
	v_pk_mul_f32 v[138:139], v[66:67], v[66:67]
	v_add_f32_e32 v124, v124, v125
	v_readlane_b32 s0, v116, 0
	v_readlane_b32 s1, v116, 32
	v_mov_b32_e32 v116, s2
	v_mov_b32_e32 v117, s3
	v_add_f32_dpp v114, v114, v114 row_mirror row_mask:0xf bank_mask:0xf bound_ctrl:1
	v_add_f32_dpp v112, v112, v112 quad_perm:[2,3,0,1] row_mask:0xf bank_mask:0xf bound_ctrl:1
	v_add_f32_e32 v110, v110, v111
	v_pk_mov_b32 v[140:141], v[138:139], v[126:127] op_sel:[1,0]
	v_mov_b32_e32 v139, v127
	v_fmamk_f32 v63, v124, 0xbb800000, v63
	v_fmac_f32_e32 v62, 0xbb800000, v124
	v_fmamk_f32 v59, v124, 0xbb800000, v59
	v_fmac_f32_e32 v58, 0xbb800000, v124
	v_pk_add_f32 v[116:117], s[0:1], v[116:117]
	v_readlane_b32 s2, v114, 16
	v_readlane_b32 s3, v114, 48
	v_add_f32_dpp v112, v112, v112 row_half_mirror row_mask:0xf bank_mask:0xf bound_ctrl:1
	v_add_f32_dpp v110, v110, v110 quad_perm:[1,0,3,2] row_mask:0xf bank_mask:0xf bound_ctrl:1
	v_pk_add_f32 v[126:127], v[140:141], v[138:139]
	v_pk_mul_f32 v[124:125], v[58:59], v[58:59]
	v_pk_mul_f32 v[138:139], v[62:63], v[62:63]
	v_add_f32_e32 v116, v116, v117
	v_readlane_b32 s0, v114, 0
	v_readlane_b32 s1, v114, 32
	v_mov_b32_e32 v114, s2
	v_mov_b32_e32 v115, s3
	v_add_f32_dpp v112, v112, v112 row_mirror row_mask:0xf bank_mask:0xf bound_ctrl:1
	v_add_f32_dpp v110, v110, v110 quad_perm:[2,3,0,1] row_mask:0xf bank_mask:0xf bound_ctrl:1
	v_add_f32_e32 v108, v108, v109
	v_pk_mov_b32 v[140:141], v[138:139], v[124:125] op_sel:[1,0]
	v_mov_b32_e32 v139, v125
	v_fmamk_f32 v55, v116, 0xbb800000, v55
	v_fmac_f32_e32 v54, 0xbb800000, v116
	v_fmamk_f32 v53, v116, 0xbb800000, v53
	v_fmac_f32_e32 v52, 0xbb800000, v116
	v_pk_add_f32 v[114:115], s[0:1], v[114:115]
	v_readlane_b32 s2, v112, 16
	v_readlane_b32 s3, v112, 48
	v_add_f32_dpp v110, v110, v110 row_half_mirror row_mask:0xf bank_mask:0xf bound_ctrl:1
	v_add_f32_dpp v108, v108, v108 quad_perm:[1,0,3,2] row_mask:0xf bank_mask:0xf bound_ctrl:1
	v_pk_add_f32 v[124:125], v[140:141], v[138:139]
	v_pk_mul_f32 v[116:117], v[52:53], v[52:53]
	v_pk_mul_f32 v[138:139], v[54:55], v[54:55]
	v_add_f32_e32 v114, v114, v115
	v_readlane_b32 s0, v112, 0
	v_readlane_b32 s1, v112, 32
	v_mov_b32_e32 v112, s2
	v_mov_b32_e32 v113, s3
	v_add_f32_dpp v110, v110, v110 row_mirror row_mask:0xf bank_mask:0xf bound_ctrl:1
	v_add_f32_dpp v108, v108, v108 quad_perm:[2,3,0,1] row_mask:0xf bank_mask:0xf bound_ctrl:1
	v_add_f32_e32 v106, v106, v107
	v_pk_mov_b32 v[140:141], v[138:139], v[116:117] op_sel:[1,0]
	v_mov_b32_e32 v139, v117
	v_fmamk_f32 v57, v114, 0xbb800000, v57
	v_fmac_f32_e32 v56, 0xbb800000, v114
	v_fmamk_f32 v51, v114, 0xbb800000, v51
	v_fmac_f32_e32 v50, 0xbb800000, v114
	v_pk_add_f32 v[112:113], s[0:1], v[112:113]
	v_readlane_b32 s2, v110, 16
	v_readlane_b32 s3, v110, 48
	v_add_f32_dpp v108, v108, v108 row_half_mirror row_mask:0xf bank_mask:0xf bound_ctrl:1
	v_add_f32_dpp v106, v106, v106 quad_perm:[1,0,3,2] row_mask:0xf bank_mask:0xf bound_ctrl:1
	v_pk_add_f32 v[116:117], v[140:141], v[138:139]
	v_pk_mul_f32 v[114:115], v[50:51], v[50:51]
	v_pk_mul_f32 v[138:139], v[56:57], v[56:57]
	v_add_f32_e32 v112, v112, v113
	v_readlane_b32 s0, v110, 0
	v_readlane_b32 s1, v110, 32
	v_mov_b32_e32 v110, s2
	v_mov_b32_e32 v111, s3
	v_add_f32_dpp v108, v108, v108 row_mirror row_mask:0xf bank_mask:0xf bound_ctrl:1
	v_add_f32_dpp v106, v106, v106 quad_perm:[2,3,0,1] row_mask:0xf bank_mask:0xf bound_ctrl:1
	v_pk_mov_b32 v[140:141], v[138:139], v[114:115] op_sel:[1,0]
	v_mov_b32_e32 v139, v115
	v_fmamk_f32 v49, v112, 0xbb800000, v49
	v_fmac_f32_e32 v48, 0xbb800000, v112
	v_fmamk_f32 v47, v112, 0xbb800000, v47
	v_fmac_f32_e32 v46, 0xbb800000, v112
	v_pk_add_f32 v[110:111], s[0:1], v[110:111]
	v_readlane_b32 s2, v108, 16
	v_readlane_b32 s3, v108, 48
	v_add_f32_dpp v106, v106, v106 row_half_mirror row_mask:0xf bank_mask:0xf bound_ctrl:1
	v_pk_add_f32 v[114:115], v[140:141], v[138:139]
	v_pk_mul_f32 v[112:113], v[46:47], v[46:47]
	v_pk_mul_f32 v[138:139], v[48:49], v[48:49]
	v_add_f32_e32 v110, v110, v111
	v_readlane_b32 s0, v108, 0
	v_readlane_b32 s1, v108, 32
	v_mov_b32_e32 v108, s2
	v_mov_b32_e32 v109, s3
	v_add_f32_dpp v106, v106, v106 row_mirror row_mask:0xf bank_mask:0xf bound_ctrl:1
	v_pk_mov_b32 v[140:141], v[138:139], v[112:113] op_sel:[1,0]
	v_mov_b32_e32 v139, v113
	v_fmamk_f32 v45, v110, 0xbb800000, v45
	v_fmac_f32_e32 v44, 0xbb800000, v110
	v_fmamk_f32 v41, v110, 0xbb800000, v41
	v_fmac_f32_e32 v40, 0xbb800000, v110
	v_pk_add_f32 v[108:109], s[0:1], v[108:109]
	v_readlane_b32 s2, v106, 16
	v_readlane_b32 s3, v106, 48
	v_pk_add_f32 v[112:113], v[140:141], v[138:139]
	v_pk_mul_f32 v[110:111], v[40:41], v[40:41]
	v_pk_mul_f32 v[138:139], v[44:45], v[44:45]
	v_add_f32_e32 v108, v108, v109
	v_readlane_b32 s0, v106, 0
	v_readlane_b32 s1, v106, 32
	v_mov_b32_e32 v106, s2
	v_mov_b32_e32 v107, s3
	v_pk_mov_b32 v[140:141], v[138:139], v[110:111] op_sel:[1,0]
	v_mov_b32_e32 v139, v111
	v_fmamk_f32 v39, v108, 0xbb800000, v39
	v_fmac_f32_e32 v38, 0xbb800000, v108
	v_fmamk_f32 v37, v108, 0xbb800000, v37
	v_fmac_f32_e32 v36, 0xbb800000, v108
	v_pk_add_f32 v[106:107], s[0:1], v[106:107]
	v_pk_add_f32 v[110:111], v[140:141], v[138:139]
	v_pk_mul_f32 v[108:109], v[36:37], v[36:37]
	v_pk_mul_f32 v[138:139], v[38:39], v[38:39]
	v_add_f32_e32 v106, v106, v107
	v_pk_mov_b32 v[140:141], v[138:139], v[108:109] op_sel:[1,0]
	v_mov_b32_e32 v139, v109
	v_fmamk_f32 v35, v106, 0xbb800000, v35
	v_fmac_f32_e32 v34, 0xbb800000, v106
	v_fmamk_f32 v31, v106, 0xbb800000, v31
	v_fmac_f32_e32 v30, 0xbb800000, v106
	v_pk_add_f32 v[108:109], v[140:141], v[138:139]
	v_pk_mul_f32 v[106:107], v[30:31], v[30:31]
	v_pk_mul_f32 v[138:139], v[34:35], v[34:35]
	v_add_f32_e32 v132, v132, v133
	v_pk_mov_b32 v[140:141], v[138:139], v[106:107] op_sel:[1,0]
	v_mov_b32_e32 v139, v107
	v_pk_add_f32 v[106:107], v[140:141], v[138:139]
	v_add_f32_e32 v122, v122, v123
	v_add_f32_e32 v133, v106, v107
	v_add_f32_dpp v106, v132, v132 quad_perm:[1,0,3,2] row_mask:0xf bank_mask:0xf bound_ctrl:1
	v_add_f32_e32 v123, v130, v131
	v_add_f32_e32 v131, v108, v109
	v_add_f32_dpp v106, v106, v106 quad_perm:[2,3,0,1] row_mask:0xf bank_mask:0xf bound_ctrl:1
	v_add_f32_e32 v118, v118, v119
	v_add_f32_e32 v130, v110, v111
	v_add_f32_dpp v106, v106, v106 row_half_mirror row_mask:0xf bank_mask:0xf bound_ctrl:1
	v_add_f32_e32 v119, v120, v121
	v_add_f32_e32 v120, v136, v137
	v_add_f32_dpp v106, v106, v106 row_mirror row_mask:0xf bank_mask:0xf bound_ctrl:1
	v_add_f32_e32 v128, v128, v129
	v_readlane_b32 s2, v106, 16
	v_readlane_b32 s3, v106, 48
	v_readlane_b32 s0, v106, 0
	v_readlane_b32 s1, v106, 32
	v_mov_b32_e32 v106, s2
	v_mov_b32_e32 v107, s3
	v_pk_add_f32 v[108:109], s[0:1], v[106:107]
	v_add_f32_dpp v106, v122, v122 quad_perm:[1,0,3,2] row_mask:0xf bank_mask:0xf bound_ctrl:1
	v_add_f32_e32 v129, v112, v113
	v_add_f32_dpp v112, v120, v120 quad_perm:[1,0,3,2] row_mask:0xf bank_mask:0xf bound_ctrl:1
	v_add_f32_dpp v106, v106, v106 quad_perm:[2,3,0,1] row_mask:0xf bank_mask:0xf bound_ctrl:1
	v_add_f32_e32 v121, v134, v135
	v_add_f32_dpp v112, v112, v112 quad_perm:[2,3,0,1] row_mask:0xf bank_mask:0xf bound_ctrl:1
	v_add_f32_dpp v106, v106, v106 row_half_mirror row_mask:0xf bank_mask:0xf bound_ctrl:1
	v_add_f32_e32 v126, v126, v127
	v_add_f32_dpp v112, v112, v112 row_half_mirror row_mask:0xf bank_mask:0xf bound_ctrl:1
	v_add_f32_dpp v106, v106, v106 row_mirror row_mask:0xf bank_mask:0xf bound_ctrl:1
	v_add_f32_e32 v127, v114, v115
	v_readlane_b32 s2, v106, 16
	v_readlane_b32 s3, v106, 48
	v_readlane_b32 s0, v106, 0
	v_readlane_b32 s1, v106, 32
	v_mov_b32_e32 v106, s2
	v_mov_b32_e32 v107, s3
	v_pk_add_f32 v[110:111], s[0:1], v[106:107]
	v_add_f32_dpp v106, v118, v118 quad_perm:[1,0,3,2] row_mask:0xf bank_mask:0xf bound_ctrl:1
	v_add_f32_dpp v112, v112, v112 row_mirror row_mask:0xf bank_mask:0xf bound_ctrl:1
	v_add_f32_dpp v114, v123, v123 quad_perm:[1,0,3,2] row_mask:0xf bank_mask:0xf bound_ctrl:1
	v_add_f32_dpp v106, v106, v106 quad_perm:[2,3,0,1] row_mask:0xf bank_mask:0xf bound_ctrl:1
	v_readlane_b32 s23, v112, 16
	v_readlane_b32 s24, v112, 48
	v_add_f32_dpp v106, v106, v106 row_half_mirror row_mask:0xf bank_mask:0xf bound_ctrl:1
	v_add_f32_dpp v114, v114, v114 quad_perm:[2,3,0,1] row_mask:0xf bank_mask:0xf bound_ctrl:1
	v_add_f32_e32 v124, v124, v125
	v_add_f32_dpp v106, v106, v106 row_mirror row_mask:0xf bank_mask:0xf bound_ctrl:1
	v_add_f32_dpp v114, v114, v114 row_half_mirror row_mask:0xf bank_mask:0xf bound_ctrl:1
	v_readlane_b32 s0, v106, 0
	v_readlane_b32 s2, v106, 16
	v_readlane_b32 s1, v106, 32
	v_readlane_b32 s3, v106, 48
	v_add_f32_dpp v106, v119, v119 quad_perm:[1,0,3,2] row_mask:0xf bank_mask:0xf bound_ctrl:1
	v_add_f32_dpp v114, v114, v114 row_mirror row_mask:0xf bank_mask:0xf bound_ctrl:1
	v_mov_b32_e32 v107, s3
	v_add_f32_dpp v106, v106, v106 quad_perm:[2,3,0,1] row_mask:0xf bank_mask:0xf bound_ctrl:1
	v_readlane_b32 s21, v114, 16
	v_readlane_b32 s22, v114, 48
	v_add_f32_dpp v106, v106, v106 row_half_mirror row_mask:0xf bank_mask:0xf bound_ctrl:1
	v_add_f32_e32 v125, v116, v117
	v_cvt_f32_f16_sdwa v115, v96 dst_sel:DWORD dst_unused:UNUSED_PAD src0_sel:WORD_1
	v_add_f32_dpp v106, v106, v106 row_mirror row_mask:0xf bank_mask:0xf bound_ctrl:1
	v_cvt_f32_f16_e32 v116, v97
	v_readlane_b32 s4, v106, 0
	v_readlane_b32 s6, v106, 16
	v_readlane_b32 s5, v106, 32
	v_readlane_b32 s7, v106, 48
	v_mov_b32_e32 v106, s2
	v_pk_add_f32 v[106:107], s[0:1], v[106:107]
	v_readlane_b32 s0, v112, 0
	v_readlane_b32 s1, v112, 32
	v_add_f32_dpp v112, v121, v121 quad_perm:[1,0,3,2] row_mask:0xf bank_mask:0xf bound_ctrl:1
	v_mov_b32_e32 v113, s7
	v_cvt_f32_f16_sdwa v117, v97 dst_sel:DWORD dst_unused:UNUSED_PAD src0_sel:WORD_1
	v_add_f32_dpp v112, v112, v112 quad_perm:[2,3,0,1] row_mask:0xf bank_mask:0xf bound_ctrl:1
	v_mov_b32_e32 v97, v108
	v_mov_b32_e32 v108, v111
	v_add_f32_dpp v112, v112, v112 row_half_mirror row_mask:0xf bank_mask:0xf bound_ctrl:1
	v_mov_b32_e32 v111, s24
	s_nop 0
	v_add_f32_dpp v112, v112, v112 row_mirror row_mask:0xf bank_mask:0xf bound_ctrl:1
	s_nop 0
	v_readlane_b32 s2, v112, 0
	v_readlane_b32 s19, v112, 16
	v_readlane_b32 s3, v112, 32
	v_readlane_b32 s20, v112, 48
	v_mov_b32_e32 v112, s6
	v_pk_add_f32 v[112:113], s[4:5], v[112:113]
	v_readlane_b32 s4, v114, 0
	v_readlane_b32 s5, v114, 32
	v_add_f32_dpp v114, v128, v128 quad_perm:[1,0,3,2] row_mask:0xf bank_mask:0xf bound_ctrl:1
	s_nop 1
	v_add_f32_dpp v114, v114, v114 quad_perm:[2,3,0,1] row_mask:0xf bank_mask:0xf bound_ctrl:1
	s_nop 1
	v_add_f32_dpp v114, v114, v114 row_half_mirror row_mask:0xf bank_mask:0xf bound_ctrl:1
	s_nop 1
	v_add_f32_dpp v114, v114, v114 row_mirror row_mask:0xf bank_mask:0xf bound_ctrl:1
	s_nop 0
	v_readlane_b32 s6, v114, 0
	v_readlane_b32 s29, v114, 16
	v_readlane_b32 s7, v114, 32
	v_readlane_b32 s30, v114, 48
	v_add_f32_dpp v114, v126, v126 quad_perm:[1,0,3,2] row_mask:0xf bank_mask:0xf bound_ctrl:1
	s_nop 1
	v_add_f32_dpp v114, v114, v114 quad_perm:[2,3,0,1] row_mask:0xf bank_mask:0xf bound_ctrl:1
	s_nop 1
	v_add_f32_dpp v114, v114, v114 row_half_mirror row_mask:0xf bank_mask:0xf bound_ctrl:1
	s_nop 1
	v_add_f32_dpp v114, v114, v114 row_mirror row_mask:0xf bank_mask:0xf bound_ctrl:1
	s_nop 0
	v_readlane_b32 s10, v114, 0
	v_readlane_b32 s31, v114, 16
	v_readlane_b32 s11, v114, 32
	v_readlane_b32 s33, v114, 48
	v_add_f32_dpp v114, v124, v124 quad_perm:[1,0,3,2] row_mask:0xf bank_mask:0xf bound_ctrl:1
	v_cvt_f32_f16_e32 v124, v69
	s_nop 0
	v_add_f32_dpp v114, v114, v114 quad_perm:[2,3,0,1] row_mask:0xf bank_mask:0xf bound_ctrl:1
	s_nop 1
	v_add_f32_dpp v114, v114, v114 row_half_mirror row_mask:0xf bank_mask:0xf bound_ctrl:1
	s_nop 1
	v_add_f32_dpp v114, v114, v114 row_mirror row_mask:0xf bank_mask:0xf bound_ctrl:1
	s_nop 0
	v_readlane_b32 s8, v114, 0
	v_readlane_b32 s34, v114, 16
	v_readlane_b32 s9, v114, 32
	v_readlane_b32 s35, v114, 48
	v_cvt_f32_f16_e32 v114, v96
	v_mov_b32_e32 v96, v110
	v_mov_b32_e32 v110, s23
	v_pk_add_f32 v[118:119], s[0:1], v[110:111]
	v_pk_add_f32 v[108:109], v[96:97], v[108:109]
	v_add_f32_dpp v110, v125, v125 quad_perm:[1,0,3,2] row_mask:0xf bank_mask:0xf bound_ctrl:1
	s_mov_b32 s0, 0x3b800000
	v_mov_b64_e32 v[96:97], s[28:29]
	v_add_f32_dpp v110, v110, v110 quad_perm:[2,3,0,1] row_mask:0xf bank_mask:0xf bound_ctrl:1
	v_cvt_f32_f16_sdwa v125, v69 dst_sel:DWORD dst_unused:UNUSED_PAD src0_sel:WORD_1
	v_mov_b32_e32 v69, v106
	v_add_f32_dpp v110, v110, v110 row_half_mirror row_mask:0xf bank_mask:0xf bound_ctrl:1
	v_mov_b32_e32 v106, v113
	s_nop 0
	v_add_f32_dpp v110, v110, v110 row_mirror row_mask:0xf bank_mask:0xf bound_ctrl:1
	s_nop 0
	v_readlane_b32 s24, v110, 0
	v_readlane_b32 s23, v110, 16
	v_readlane_b32 s25, v110, 32
	v_readlane_b32 s36, v110, 48
	v_add_f32_dpp v110, v127, v127 quad_perm:[1,0,3,2] row_mask:0xf bank_mask:0xf bound_ctrl:1
	s_nop 1
	v_add_f32_dpp v110, v110, v110 quad_perm:[2,3,0,1] row_mask:0xf bank_mask:0xf bound_ctrl:1
	s_nop 1
	v_add_f32_dpp v110, v110, v110 row_half_mirror row_mask:0xf bank_mask:0xf bound_ctrl:1
	s_nop 1
	v_add_f32_dpp v120, v110, v110 row_mirror row_mask:0xf bank_mask:0xf bound_ctrl:1
	v_pk_fma_f32 v[110:111], v[108:109], s[0:1], v[96:97] op_sel_hi:[1,0,0]
	s_mov_b32 s1, 0x800000
	v_mul_f32_e32 v108, 0x4b800000, v111
	v_cmp_gt_f32_e32 vcc, s1, v111
	v_readlane_b32 s26, v120, 0
	v_readlane_b32 s28, v120, 16
	v_cndmask_b32_e32 v108, v111, v108, vcc
	v_rsq_f32_e32 v108, v108
	v_readlane_b32 s27, v120, 32
	v_readlane_b32 s37, v120, 48
	v_mul_f32_e32 v109, 0x45800000, v108
	v_cndmask_b32_e32 v108, v108, v109, vcc
	v_pk_mul_f32 v[104:105], v[108:109], v[104:105] op_sel_hi:[0,1]
	v_pk_mul_f32 v[102:103], v[108:109], v[102:103] op_sel_hi:[0,1]
	v_pk_fma_f32 v[104:105], v[0:1], v[104:105], v[4:5]
	v_pk_fma_f32 v[102:103], v[2:3], v[102:103], v[6:7]
	v_pk_mul_f32 v[104:105], v[104:105], v[114:115]
	v_mov_b32_e32 v114, s19
	v_mov_b32_e32 v115, s20
	v_mov_b32_e32 v108, s21
	v_mov_b32_e32 v109, s22
	v_pk_mul_f32 v[102:103], v[102:103], v[116:117]
	v_pk_add_f32 v[120:121], s[2:3], v[114:115]
	v_pk_add_f32 v[114:115], s[4:5], v[108:109]
	v_mov_b32_e32 v108, s29
	v_mov_b32_e32 v109, s30
	v_cvt_pk_f16_f32 v104, v104, v105
	v_cvt_pk_f16_f32 v105, v102, v103
	v_mov_b32_e32 v102, s31
	v_mov_b32_e32 v103, s33
	v_pk_add_f32 v[116:117], s[6:7], v[108:109]
	v_pk_add_f32 v[108:109], s[10:11], v[102:103]
	v_add_f32_dpp v102, v129, v129 quad_perm:[1,0,3,2] row_mask:0xf bank_mask:0xf bound_ctrl:1
	v_cmp_gt_f32_e32 vcc, s1, v110
	v_mov_b32_e32 v103, s35
	v_add_f32_dpp v102, v102, v102 quad_perm:[2,3,0,1] row_mask:0xf bank_mask:0xf bound_ctrl:1
	global_store_dwordx2 v[60:61], v[104:105], off
	v_mov_b32_e32 v105, s37
	v_add_f32_dpp v102, v102, v102 row_half_mirror row_mask:0xf bank_mask:0xf bound_ctrl:1
	s_nop 1
	v_add_f32_dpp v102, v102, v102 row_mirror row_mask:0xf bank_mask:0xf bound_ctrl:1
	s_nop 0
	v_readlane_b32 s2, v102, 0
	v_readlane_b32 s6, v102, 16
	v_readlane_b32 s3, v102, 32
	v_readlane_b32 s7, v102, 48
	v_mul_f32_e32 v102, 0x4b800000, v110
	v_cndmask_b32_e32 v122, v110, v102, vcc
	v_mov_b32_e32 v102, s34
	v_rsq_f32_e32 v122, v122
	v_pk_add_f32 v[110:111], s[8:9], v[102:103]
	v_add_f32_dpp v102, v130, v130 quad_perm:[1,0,3,2] row_mask:0xf bank_mask:0xf bound_ctrl:1
	v_cvt_f32_f16_sdwa v103, v70 dst_sel:DWORD dst_unused:UNUSED_PAD src0_sel:WORD_1
	v_mul_f32_e32 v104, 0x45800000, v122
	v_add_f32_dpp v102, v102, v102 quad_perm:[2,3,0,1] row_mask:0xf bank_mask:0xf bound_ctrl:1
	s_nop 1
	v_add_f32_dpp v102, v102, v102 row_half_mirror row_mask:0xf bank_mask:0xf bound_ctrl:1
	s_nop 1
	v_add_f32_dpp v102, v102, v102 row_mirror row_mask:0xf bank_mask:0xf bound_ctrl:1
	s_nop 0
	v_readlane_b32 s4, v102, 0
	v_readlane_b32 s8, v102, 16
	v_readlane_b32 s5, v102, 32
	v_readlane_b32 s9, v102, 48
	v_cvt_f32_f16_e32 v102, v70
	v_cndmask_b32_e32 v70, v122, v104, vcc
	v_pk_mul_f32 v[100:101], v[70:71], v[100:101] op_sel_hi:[0,1]
	v_pk_mul_f32 v[98:99], v[70:71], v[98:99] op_sel_hi:[0,1]
	v_cvt_f32_f16_e32 v70, v71
	v_cvt_f32_f16_sdwa v71, v71 dst_sel:DWORD dst_unused:UNUSED_PAD src0_sel:WORD_1
	v_pk_fma_f32 v[100:101], v[0:1], v[100:101], v[4:5]
	v_pk_fma_f32 v[98:99], v[2:3], v[98:99], v[6:7]
	v_pk_mul_f32 v[100:101], v[100:101], v[102:103]
	v_pk_mul_f32 v[70:71], v[98:99], v[70:71]
	v_cvt_pk_f16_f32 v100, v100, v101
	v_cvt_pk_f16_f32 v101, v70, v71
	v_cvt_f32_f16_e32 v70, v68
	v_cvt_f32_f16_sdwa v71, v68 dst_sel:DWORD dst_unused:UNUSED_PAD src0_sel:WORD_1
	v_mov_b32_e32 v68, v112
	v_pk_add_f32 v[68:69], v[68:69], v[106:107]
	v_add_f32_dpp v106, v131, v131 quad_perm:[1,0,3,2] row_mask:0xf bank_mask:0xf bound_ctrl:1
	v_mov_b32_e32 v98, s6
	v_mov_b32_e32 v99, s7
	v_add_f32_dpp v106, v106, v106 quad_perm:[2,3,0,1] row_mask:0xf bank_mask:0xf bound_ctrl:1
	v_pk_add_f32 v[98:99], s[2:3], v[98:99]
	v_add_co_u32_e32 v122, vcc, s18, v60
	v_add_f32_dpp v106, v106, v106 row_half_mirror row_mask:0xf bank_mask:0xf bound_ctrl:1
	s_nop 0
	v_addc_co_u32_e32 v123, vcc, 0, v61, vcc
	v_add_f32_dpp v106, v106, v106 row_mirror row_mask:0xf bank_mask:0xf bound_ctrl:1
	global_store_dwordx2 v[122:123], v[100:101], off offset:-4096
	v_readlane_b32 s2, v106, 0
	v_readlane_b32 s6, v106, 16
	v_readlane_b32 s3, v106, 32
	v_readlane_b32 s7, v106, 48
	v_add_f32_dpp v106, v133, v133 quad_perm:[1,0,3,2] row_mask:0xf bank_mask:0xf bound_ctrl:1
	v_mov_b32_e32 v100, s8
	v_mov_b32_e32 v101, s9
	v_add_f32_dpp v106, v106, v106 quad_perm:[2,3,0,1] row_mask:0xf bank_mask:0xf bound_ctrl:1
	v_pk_add_f32 v[100:101], s[4:5], v[100:101]
	v_mov_b32_e32 v102, s23
	v_add_f32_dpp v106, v106, v106 row_half_mirror row_mask:0xf bank_mask:0xf bound_ctrl:1
	v_mov_b32_e32 v103, s36
	v_mov_b32_e32 v104, s28
	v_add_f32_dpp v112, v106, v106 row_mirror row_mask:0xf bank_mask:0xf bound_ctrl:1
	v_pk_fma_f32 v[106:107], v[68:69], s[0:1], v[96:97] op_sel_hi:[1,0,0]
	v_readlane_b32 s4, v112, 0
	v_mul_f32_e32 v68, 0x4b800000, v107
	v_cmp_gt_f32_e32 vcc, s1, v107
	v_readlane_b32 s8, v112, 16
	v_readlane_b32 s5, v112, 32
	v_cndmask_b32_e32 v68, v107, v68, vcc
	v_rsq_f32_e32 v68, v68
	v_readlane_b32 s9, v112, 48
	v_pk_add_f32 v[102:103], s[24:25], v[102:103]
	v_pk_add_f32 v[104:105], s[26:27], v[104:105]
	v_mul_f32_e32 v69, 0x45800000, v68
	v_cndmask_b32_e32 v112, v68, v69, vcc
	v_pk_mul_f32 v[68:69], v[112:113], v[94:95] op_sel_hi:[0,1]
	v_pk_fma_f32 v[68:69], v[0:1], v[68:69], v[4:5]
	v_cmp_gt_f32_e32 vcc, s1, v106
	v_pk_mul_f32 v[94:95], v[68:69], v[70:71]
	v_mul_f32_e32 v70, 0x4b800000, v106
	v_cndmask_b32_e32 v106, v106, v70, vcc
	v_pk_mul_f32 v[92:93], v[112:113], v[92:93] op_sel_hi:[0,1]
	v_rsq_f32_e32 v106, v106
	v_pk_fma_f32 v[92:93], v[2:3], v[92:93], v[6:7]
	v_cvt_pk_f16_f32 v94, v94, v95
	v_pk_mul_f32 v[92:93], v[92:93], v[124:125]
	v_mov_b32_e32 v68, s6
	v_cvt_pk_f16_f32 v95, v92, v93
	global_store_dwordx2 v[122:123], v[94:95], off
	v_mul_f32_e32 v94, 0x45800000, v106
	v_cvt_f32_f16_e32 v92, v42
	v_cvt_f32_f16_sdwa v93, v42 dst_sel:DWORD dst_unused:UNUSED_PAD src0_sel:WORD_1
	v_cndmask_b32_e32 v42, v106, v94, vcc
	v_pk_mul_f32 v[90:91], v[42:43], v[90:91] op_sel_hi:[0,1]
	v_pk_fma_f32 v[90:91], v[0:1], v[90:91], v[4:5]
	v_mov_b32_e32 v69, s7
	v_pk_mul_f32 v[90:91], v[90:91], v[92:93]
	v_cvt_f32_f16_e32 v92, v43
	v_cvt_f32_f16_sdwa v93, v43 dst_sel:DWORD dst_unused:UNUSED_PAD src0_sel:WORD_1
	v_pk_mul_f32 v[42:43], v[42:43], v[88:89] op_sel_hi:[0,1]
	v_pk_fma_f32 v[42:43], v[2:3], v[42:43], v[6:7]
	v_cvt_pk_f16_f32 v90, v90, v91
	v_pk_mul_f32 v[42:43], v[42:43], v[92:93]
	v_cvt_f32_f16_e32 v88, v32
	v_cvt_pk_f16_f32 v91, v42, v43
	v_add_co_u32_e32 v42, vcc, s17, v60
	v_mov_b32_e32 v70, s8
	s_nop 0
	v_addc_co_u32_e32 v43, vcc, 0, v61, vcc
	global_store_dwordx2 v[42:43], v[90:91], off offset:-4096
	v_mov_b32_e32 v90, v120
	v_mov_b32_e32 v91, v118
	v_mov_b32_e32 v118, v121
	v_pk_add_f32 v[90:91], v[90:91], v[118:119]
	v_mov_b32_e32 v71, s9
	v_pk_fma_f32 v[90:91], v[90:91], s[0:1], v[96:97] op_sel_hi:[1,0,0]
	v_pk_add_f32 v[68:69], s[2:3], v[68:69]
	v_mul_f32_e32 v89, 0x4b800000, v91
	v_cmp_gt_f32_e32 vcc, s1, v91
	v_pk_add_f32 v[70:71], s[4:5], v[70:71]
	s_nop 0
	v_cndmask_b32_e32 v89, v91, v89, vcc
	v_rsq_f32_e32 v91, v89
	v_cvt_f32_f16_sdwa v89, v32 dst_sel:DWORD dst_unused:UNUSED_PAD src0_sel:WORD_1
	v_cvt_f32_f16_e32 v32, v33
	v_cvt_f32_f16_sdwa v33, v33 dst_sel:DWORD dst_unused:UNUSED_PAD src0_sel:WORD_1
	v_mul_f32_e32 v92, 0x45800000, v91
	v_cndmask_b32_e32 v92, v91, v92, vcc
	v_pk_mul_f32 v[86:87], v[92:93], v[86:87] op_sel_hi:[0,1]
	v_pk_fma_f32 v[86:87], v[0:1], v[86:87], v[4:5]
	v_cmp_gt_f32_e32 vcc, s1, v90
	v_pk_mul_f32 v[86:87], v[86:87], v[88:89]
	v_pk_mul_f32 v[84:85], v[92:93], v[84:85] op_sel_hi:[0,1]
	v_cvt_pk_f16_f32 v86, v86, v87
	v_mul_f32_e32 v87, 0x4b800000, v90
	v_cndmask_b32_e32 v87, v90, v87, vcc
	v_rsq_f32_e32 v88, v87
	v_pk_fma_f32 v[84:85], v[2:3], v[84:85], v[6:7]
	s_nop 0
	v_pk_mul_f32 v[32:33], v[84:85], v[32:33]
	s_nop 0
	v_cvt_pk_f16_f32 v87, v32, v33
	global_store_dwordx2 v[42:43], v[86:87], off
	v_mul_f32_e32 v42, 0x45800000, v88
	v_cvt_f32_f16_e32 v32, v28
	v_cvt_f32_f16_sdwa v33, v28 dst_sel:DWORD dst_unused:UNUSED_PAD src0_sel:WORD_1
	v_cndmask_b32_e32 v28, v88, v42, vcc
	v_pk_mul_f32 v[42:43], v[28:29], v[82:83] op_sel_hi:[0,1]
	v_pk_fma_f32 v[42:43], v[0:1], v[42:43], v[4:5]
	s_nop 0
	v_pk_mul_f32 v[32:33], v[42:43], v[32:33]
	v_cvt_f32_f16_e32 v42, v29
	v_cvt_f32_f16_sdwa v43, v29 dst_sel:DWORD dst_unused:UNUSED_PAD src0_sel:WORD_1
	v_pk_mul_f32 v[28:29], v[28:29], v[80:81] op_sel_hi:[0,1]
	v_pk_fma_f32 v[28:29], v[2:3], v[28:29], v[6:7]
	v_cvt_pk_f16_f32 v32, v32, v33
	v_pk_mul_f32 v[28:29], v[28:29], v[42:43]
	v_mov_b32_e32 v42, v116
	v_mov_b32_e32 v43, v114
	v_mov_b32_e32 v114, v117
	v_cvt_pk_f16_f32 v33, v28, v29
	v_add_co_u32_e32 v28, vcc, s16, v60
	v_pk_add_f32 v[42:43], v[42:43], v[114:115]
	s_nop 0
	v_addc_co_u32_e32 v29, vcc, 0, v61, vcc
	v_pk_fma_f32 v[42:43], v[42:43], s[0:1], v[96:97] op_sel_hi:[1,0,0]
	global_store_dwordx2 v[28:29], v[32:33], off offset:-4096
	v_mul_f32_e32 v33, 0x4b800000, v43
	v_cmp_gt_f32_e32 vcc, s1, v43
	v_cvt_f32_f16_e32 v32, v26
	s_nop 0
	v_cndmask_b32_e32 v33, v43, v33, vcc
	v_rsq_f32_e32 v43, v33
	v_cvt_f32_f16_sdwa v33, v26 dst_sel:DWORD dst_unused:UNUSED_PAD src0_sel:WORD_1
	v_cvt_f32_f16_e32 v26, v27
	v_cvt_f32_f16_sdwa v27, v27 dst_sel:DWORD dst_unused:UNUSED_PAD src0_sel:WORD_1
	v_mul_f32_e32 v80, 0x45800000, v43
	v_cndmask_b32_e32 v80, v43, v80, vcc
	v_pk_mul_f32 v[76:77], v[80:81], v[76:77] op_sel_hi:[0,1]
	v_pk_fma_f32 v[76:77], v[0:1], v[76:77], v[4:5]
	v_cmp_gt_f32_e32 vcc, s1, v42
	v_pk_mul_f32 v[32:33], v[76:77], v[32:33]
	v_pk_mul_f32 v[74:75], v[80:81], v[74:75] op_sel_hi:[0,1]
	v_cvt_pk_f16_f32 v32, v32, v33
	v_mul_f32_e32 v33, 0x4b800000, v42
	v_cndmask_b32_e32 v33, v42, v33, vcc
	v_rsq_f32_e32 v42, v33
	v_pk_fma_f32 v[74:75], v[2:3], v[74:75], v[6:7]
	s_nop 0
	v_pk_mul_f32 v[26:27], v[74:75], v[26:27]
	s_nop 0
	v_cvt_pk_f16_f32 v33, v26, v27
	global_store_dwordx2 v[28:29], v[32:33], off
	v_mul_f32_e32 v28, 0x45800000, v42
	v_cvt_f32_f16_e32 v26, v24
	v_cvt_f32_f16_sdwa v27, v24 dst_sel:DWORD dst_unused:UNUSED_PAD src0_sel:WORD_1
	v_cndmask_b32_e32 v24, v42, v28, vcc
	v_pk_mul_f32 v[28:29], v[24:25], v[78:79] op_sel_hi:[0,1]
	v_pk_fma_f32 v[28:29], v[0:1], v[28:29], v[4:5]
	s_nop 0
	v_pk_mul_f32 v[26:27], v[28:29], v[26:27]
	v_cvt_f32_f16_e32 v28, v25
	v_cvt_f32_f16_sdwa v29, v25 dst_sel:DWORD dst_unused:UNUSED_PAD src0_sel:WORD_1
	v_pk_mul_f32 v[24:25], v[24:25], v[72:73] op_sel_hi:[0,1]
	v_pk_fma_f32 v[24:25], v[2:3], v[24:25], v[6:7]
	v_cvt_pk_f16_f32 v26, v26, v27
	v_pk_mul_f32 v[24:25], v[24:25], v[28:29]
	v_mov_b32_e32 v28, v110
	v_mov_b32_e32 v29, v108
	v_mov_b32_e32 v108, v111
	v_cvt_pk_f16_f32 v27, v24, v25
	v_add_co_u32_e32 v24, vcc, s15, v60
	v_pk_add_f32 v[28:29], v[28:29], v[108:109]
	s_nop 0
	v_addc_co_u32_e32 v25, vcc, 0, v61, vcc
	v_pk_fma_f32 v[28:29], v[28:29], s[0:1], v[96:97] op_sel_hi:[1,0,0]
	global_store_dwordx2 v[24:25], v[26:27], off offset:-4096
	v_mul_f32_e32 v27, 0x4b800000, v29
	v_cmp_gt_f32_e32 vcc, s1, v29
	v_cvt_f32_f16_e32 v26, v22
	s_nop 0
	v_cndmask_b32_e32 v27, v29, v27, vcc
	v_rsq_f32_e32 v29, v27
	v_cvt_f32_f16_sdwa v27, v22 dst_sel:DWORD dst_unused:UNUSED_PAD src0_sel:WORD_1
	v_cvt_f32_f16_e32 v22, v23
	v_cvt_f32_f16_sdwa v23, v23 dst_sel:DWORD dst_unused:UNUSED_PAD src0_sel:WORD_1
	v_mul_f32_e32 v32, 0x45800000, v29
	v_cndmask_b32_e32 v32, v29, v32, vcc
	v_pk_mul_f32 v[42:43], v[32:33], v[66:67] op_sel_hi:[0,1]
	v_pk_fma_f32 v[42:43], v[0:1], v[42:43], v[4:5]
	v_cmp_gt_f32_e32 vcc, s1, v28
	v_pk_mul_f32 v[26:27], v[42:43], v[26:27]
	v_pk_mul_f32 v[32:33], v[32:33], v[64:65] op_sel_hi:[0,1]
	v_cvt_pk_f16_f32 v26, v26, v27
	v_mul_f32_e32 v27, 0x4b800000, v28
	v_cndmask_b32_e32 v27, v28, v27, vcc
	v_rsq_f32_e32 v28, v27
	v_pk_fma_f32 v[32:33], v[2:3], v[32:33], v[6:7]
	s_nop 0
	v_pk_mul_f32 v[22:23], v[32:33], v[22:23]
	s_nop 0
	v_cvt_pk_f16_f32 v27, v22, v23
	global_store_dwordx2 v[24:25], v[26:27], off
	v_mul_f32_e32 v24, 0x45800000, v28
	v_cvt_f32_f16_e32 v22, v20
	v_cvt_f32_f16_sdwa v23, v20 dst_sel:DWORD dst_unused:UNUSED_PAD src0_sel:WORD_1
	v_cndmask_b32_e32 v20, v28, v24, vcc
	v_pk_mul_f32 v[24:25], v[20:21], v[62:63] op_sel_hi:[0,1]
	v_pk_fma_f32 v[24:25], v[0:1], v[24:25], v[4:5]
	s_nop 0
	v_pk_mul_f32 v[22:23], v[24:25], v[22:23]
	v_cvt_f32_f16_e32 v24, v21
	v_cvt_f32_f16_sdwa v25, v21 dst_sel:DWORD dst_unused:UNUSED_PAD src0_sel:WORD_1
	v_pk_mul_f32 v[20:21], v[20:21], v[58:59] op_sel_hi:[0,1]
	v_pk_fma_f32 v[20:21], v[2:3], v[20:21], v[6:7]
	v_cvt_pk_f16_f32 v22, v22, v23
	v_pk_mul_f32 v[20:21], v[20:21], v[24:25]
	v_mov_b32_e32 v24, v104
	v_mov_b32_e32 v25, v102
	v_mov_b32_e32 v102, v105
	v_cvt_pk_f16_f32 v23, v20, v21
	v_add_co_u32_e32 v20, vcc, s14, v60
	v_pk_add_f32 v[24:25], v[24:25], v[102:103]
	s_nop 0
	v_addc_co_u32_e32 v21, vcc, 0, v61, vcc
	v_pk_fma_f32 v[24:25], v[24:25], s[0:1], v[96:97] op_sel_hi:[1,0,0]
	global_store_dwordx2 v[20:21], v[22:23], off offset:-4096
	v_mul_f32_e32 v23, 0x4b800000, v25
	v_cmp_gt_f32_e32 vcc, s1, v25
	v_cvt_f32_f16_e32 v22, v18
	s_nop 0
	v_cndmask_b32_e32 v23, v25, v23, vcc
	v_rsq_f32_e32 v25, v23
	v_cvt_f32_f16_sdwa v23, v18 dst_sel:DWORD dst_unused:UNUSED_PAD src0_sel:WORD_1
	v_cvt_f32_f16_e32 v18, v19
	v_cvt_f32_f16_sdwa v19, v19 dst_sel:DWORD dst_unused:UNUSED_PAD src0_sel:WORD_1
	v_mul_f32_e32 v26, 0x45800000, v25
	v_cndmask_b32_e32 v26, v25, v26, vcc
	v_pk_mul_f32 v[28:29], v[26:27], v[54:55] op_sel_hi:[0,1]
	v_pk_fma_f32 v[28:29], v[0:1], v[28:29], v[4:5]
	v_cmp_gt_f32_e32 vcc, s1, v24
	v_pk_mul_f32 v[22:23], v[28:29], v[22:23]
	v_pk_mul_f32 v[26:27], v[26:27], v[52:53] op_sel_hi:[0,1]
	v_cvt_pk_f16_f32 v22, v22, v23
	v_mul_f32_e32 v23, 0x4b800000, v24
	v_cndmask_b32_e32 v23, v24, v23, vcc
	v_rsq_f32_e32 v24, v23
	v_pk_fma_f32 v[26:27], v[2:3], v[26:27], v[6:7]
	s_nop 0
	v_pk_mul_f32 v[18:19], v[26:27], v[18:19]
	s_nop 0
	v_cvt_pk_f16_f32 v23, v18, v19
	global_store_dwordx2 v[20:21], v[22:23], off
	v_mul_f32_e32 v20, 0x45800000, v24
	v_cvt_f32_f16_e32 v18, v16
	v_cvt_f32_f16_sdwa v19, v16 dst_sel:DWORD dst_unused:UNUSED_PAD src0_sel:WORD_1
	v_cndmask_b32_e32 v16, v24, v20, vcc
	v_pk_mul_f32 v[20:21], v[16:17], v[56:57] op_sel_hi:[0,1]
	v_pk_fma_f32 v[20:21], v[0:1], v[20:21], v[4:5]
	s_nop 0
	v_pk_mul_f32 v[18:19], v[20:21], v[18:19]
	v_cvt_f32_f16_e32 v20, v17
	v_cvt_f32_f16_sdwa v21, v17 dst_sel:DWORD dst_unused:UNUSED_PAD src0_sel:WORD_1
	v_pk_mul_f32 v[16:17], v[16:17], v[50:51] op_sel_hi:[0,1]
	v_pk_fma_f32 v[16:17], v[2:3], v[16:17], v[6:7]
	v_cvt_pk_f16_f32 v18, v18, v19
	v_pk_mul_f32 v[16:17], v[16:17], v[20:21]
	v_mov_b32_e32 v20, v100
	v_mov_b32_e32 v21, v98
	v_mov_b32_e32 v98, v101
	v_cvt_pk_f16_f32 v19, v16, v17
	v_add_co_u32_e32 v16, vcc, s13, v60
	v_pk_add_f32 v[20:21], v[20:21], v[98:99]
	s_nop 0
	v_addc_co_u32_e32 v17, vcc, 0, v61, vcc
	v_pk_fma_f32 v[20:21], v[20:21], s[0:1], v[96:97] op_sel_hi:[1,0,0]
	global_store_dwordx2 v[16:17], v[18:19], off offset:-4096
	v_mul_f32_e32 v19, 0x4b800000, v21
	v_cmp_gt_f32_e32 vcc, s1, v21
	v_cvt_f32_f16_e32 v18, v14
	s_nop 0
	v_cndmask_b32_e32 v19, v21, v19, vcc
	v_rsq_f32_e32 v21, v19
	v_cvt_f32_f16_sdwa v19, v14 dst_sel:DWORD dst_unused:UNUSED_PAD src0_sel:WORD_1
	v_cvt_f32_f16_e32 v14, v15
	v_cvt_f32_f16_sdwa v15, v15 dst_sel:DWORD dst_unused:UNUSED_PAD src0_sel:WORD_1
	v_mul_f32_e32 v22, 0x45800000, v21
	v_cndmask_b32_e32 v22, v21, v22, vcc
	v_pk_mul_f32 v[24:25], v[22:23], v[48:49] op_sel_hi:[0,1]
	v_pk_fma_f32 v[24:25], v[0:1], v[24:25], v[4:5]
	v_cmp_gt_f32_e32 vcc, s1, v20
	v_pk_mul_f32 v[18:19], v[24:25], v[18:19]
	v_pk_mul_f32 v[22:23], v[22:23], v[46:47] op_sel_hi:[0,1]
	v_cvt_pk_f16_f32 v18, v18, v19
	v_mul_f32_e32 v19, 0x4b800000, v20
	v_cndmask_b32_e32 v19, v20, v19, vcc
	v_rsq_f32_e32 v20, v19
	v_pk_fma_f32 v[22:23], v[2:3], v[22:23], v[6:7]
	s_nop 0
	v_pk_mul_f32 v[14:15], v[22:23], v[14:15]
	s_nop 0
	v_cvt_pk_f16_f32 v19, v14, v15
	global_store_dwordx2 v[16:17], v[18:19], off
	v_mul_f32_e32 v16, 0x45800000, v20
	v_cvt_f32_f16_e32 v14, v12
	v_cvt_f32_f16_sdwa v15, v12 dst_sel:DWORD dst_unused:UNUSED_PAD src0_sel:WORD_1
	v_cndmask_b32_e32 v12, v20, v16, vcc
	v_pk_mul_f32 v[16:17], v[12:13], v[44:45] op_sel_hi:[0,1]
	v_pk_fma_f32 v[16:17], v[0:1], v[16:17], v[4:5]
	s_nop 0
	v_pk_mul_f32 v[14:15], v[16:17], v[14:15]
	v_cvt_f32_f16_e32 v16, v13
	v_cvt_f32_f16_sdwa v17, v13 dst_sel:DWORD dst_unused:UNUSED_PAD src0_sel:WORD_1
	v_pk_mul_f32 v[12:13], v[12:13], v[40:41] op_sel_hi:[0,1]
	v_pk_fma_f32 v[12:13], v[2:3], v[12:13], v[6:7]
	v_cvt_pk_f16_f32 v14, v14, v15
	v_pk_mul_f32 v[12:13], v[12:13], v[16:17]
	v_mov_b32_e32 v16, v70
	v_mov_b32_e32 v17, v68
	v_mov_b32_e32 v68, v71
	v_cvt_pk_f16_f32 v15, v12, v13
	v_add_co_u32_e32 v12, vcc, s12, v60
	v_pk_add_f32 v[16:17], v[16:17], v[68:69]
	s_nop 0
	v_addc_co_u32_e32 v13, vcc, 0, v61, vcc
	v_pk_fma_f32 v[16:17], v[16:17], s[0:1], v[96:97] op_sel_hi:[1,0,0]
	global_store_dwordx2 v[12:13], v[14:15], off offset:-4096
	v_mul_f32_e32 v15, 0x4b800000, v17
	v_cmp_gt_f32_e32 vcc, s1, v17
	v_cvt_f32_f16_e32 v14, v10
	s_nop 0
	v_cndmask_b32_e32 v15, v17, v15, vcc
	v_rsq_f32_e32 v17, v15
	v_cvt_f32_f16_sdwa v15, v10 dst_sel:DWORD dst_unused:UNUSED_PAD src0_sel:WORD_1
	v_cvt_f32_f16_e32 v10, v11
	v_cvt_f32_f16_sdwa v11, v11 dst_sel:DWORD dst_unused:UNUSED_PAD src0_sel:WORD_1
	v_mul_f32_e32 v18, 0x45800000, v17
	v_cndmask_b32_e32 v18, v17, v18, vcc
	v_pk_mul_f32 v[20:21], v[18:19], v[38:39] op_sel_hi:[0,1]
	v_pk_fma_f32 v[20:21], v[0:1], v[20:21], v[4:5]
	v_cmp_gt_f32_e32 vcc, s1, v16
	v_pk_mul_f32 v[14:15], v[20:21], v[14:15]
	v_pk_mul_f32 v[18:19], v[18:19], v[36:37] op_sel_hi:[0,1]
	v_cvt_pk_f16_f32 v14, v14, v15
	v_mul_f32_e32 v15, 0x4b800000, v16
	v_cndmask_b32_e32 v15, v16, v15, vcc
	v_rsq_f32_e32 v16, v15
	v_pk_fma_f32 v[18:19], v[2:3], v[18:19], v[6:7]
	s_nop 0
	v_pk_mul_f32 v[10:11], v[18:19], v[10:11]
	s_nop 0
	v_cvt_pk_f16_f32 v15, v10, v11
	global_store_dwordx2 v[12:13], v[14:15], off
	v_mul_f32_e32 v12, 0x45800000, v16
	v_cvt_f32_f16_e32 v10, v8
	v_cvt_f32_f16_sdwa v11, v8 dst_sel:DWORD dst_unused:UNUSED_PAD src0_sel:WORD_1
	v_cndmask_b32_e32 v8, v16, v12, vcc
	v_pk_mul_f32 v[12:13], v[8:9], v[34:35] op_sel_hi:[0,1]
	v_pk_fma_f32 v[0:1], v[0:1], v[12:13], v[4:5]
	v_cvt_f32_f16_e32 v4, v9
	v_cvt_f32_f16_sdwa v5, v9 dst_sel:DWORD dst_unused:UNUSED_PAD src0_sel:WORD_1
	v_pk_mul_f32 v[8:9], v[8:9], v[30:31] op_sel_hi:[0,1]
	v_pk_fma_f32 v[2:3], v[2:3], v[8:9], v[6:7]
	v_pk_mul_f32 v[0:1], v[0:1], v[10:11]
	v_pk_mul_f32 v[2:3], v[2:3], v[4:5]
	v_cvt_pk_f16_f32 v0, v0, v1
	v_cvt_pk_f16_f32 v1, v2, v3
	v_add_co_u32_e32 v2, vcc, 0xf000, v60
	s_nop 1
	v_addc_co_u32_e32 v3, vcc, 0, v61, vcc
	global_store_dwordx2 v[2:3], v[0:1], off
	s_endpgm
	.p2align	8

.LBB4_398:
	v_cvt_pk_f16_f32 v7, v6, v7
	v_cvt_pk_f16_f32 v6, v4, v5
	v_cvt_pk_f16_f32 v4, v0, v1
	v_lshl_add_u64 v[0:1], s[4:5], 0, v[32:33]
	v_mov_b32_e32 v129, 0
	v_cvt_pk_f16_f32 v5, v2, v3
	v_lshl_add_u64 v[0:1], v[0:1], 0, v[128:129]
	global_store_dwordx4 v[0:1], v[4:7], off offset:256
	s_endpgm
	.p2align	8

.LBB5_6:
	s_or_b64 exec, exec, s[4:5]
	s_add_i32 s4, s2, 1
	s_ashr_i32 s5, s4, 31
	s_lshl_b64 s[4:5], s[4:5], 7
	s_add_u32 s22, s13, s4
	s_addc_u32 s23, s14, s5
	s_add_i32 s10, 0, 0x18000
	v_add_u32_e32 v170, s10, v1
	v_lshl_add_u64 v[4:5], s[22:23], 0, v[134:135]
	v_readfirstlane_b32 s20, v170
	s_mov_b32 m0, s20
	v_add_u32_e32 v2, 0x2000, v170
	s_waitcnt vmcnt(2)
	s_barrier
	global_load_lds_dwordx4 v[4:5], off
	v_lshl_add_u64 v[4:5], s[22:23], 0, v[136:137]
	v_readfirstlane_b32 s20, v2
	s_add_u32 s22, s15, s4
	v_add_u32_e32 v2, 0x8000, v146
	s_mov_b32 m0, s20
	s_addc_u32 s23, s16, s5
	v_readfirstlane_b32 s20, v2
	v_add_u32_e32 v2, 0xa000, v146
	global_load_lds_dwordx4 v[4:5], off
	v_lshl_add_u64 v[4:5], v[130:131], 1, s[22:23]
	s_mov_b32 m0, s20
	v_readfirstlane_b32 s20, v2
	s_add_u32 s4, s17, s4
	global_load_lds_dwordx4 v[4:5], off
	s_mov_b32 m0, s20
	s_addc_u32 s5, s18, s5
	s_add_i32 s20, 0, 0x1c000
	v_add_u32_e32 v171, s20, v1
	v_lshl_add_u64 v[4:5], v[132:133], 1, s[22:23]
	v_readfirstlane_b32 s22, v171
	global_load_lds_dwordx4 v[4:5], off
	v_lshl_add_u64 v[4:5], s[4:5], 0, v[134:135]
	s_mov_b32 m0, s22
	v_add_u32_e32 v1, 0x2000, v171
	global_load_lds_dwordx4 v[4:5], off
	v_lshl_add_u64 v[4:5], s[4:5], 0, v[136:137]
	v_readfirstlane_b32 s4, v1
	s_mov_b32 m0, s4
	v_lshlrev_b32_e32 v1, 6, v0
	global_load_lds_dwordx4 v[4:5], off
	v_lshlrev_b32_e32 v2, 2, v0
	s_waitcnt vmcnt(6)
	v_and_b32_e32 v173, 48, v0
	v_and_b32_e32 v1, 0x3c0, v1
	v_and_b32_e32 v2, 32, v2
	v_bfe_u32 v144, v0, 6, 2
	v_bitop3_b32 v2, v1, v2, v173 bitop3:0x36
	v_lshlrev_b32_e32 v145, 6, v3
	v_and_b32_e32 v143, 15, v0
	s_cmp_gt_i32 s11, 2
	v_add_u32_e32 v153, s19, v2
	v_add_u32_e32 v151, s21, v2
	v_lshlrev_b32_e32 v1, 12, v144
	v_lshlrev_b32_e32 v168, 13, v3
	v_or_b32_e32 v176, 16, v145
	v_or_b32_e32 v175, 32, v145
	v_or_b32_e32 v174, 48, v145
	s_barrier
	s_cbranch_scc1 .LBB5_8
	v_lshlrev_b32_e32 v172, 13, v3
	v_or_b32_e32 v3, v176, v143
	v_lshlrev_b32_e32 v4, 6, v3
	v_lshlrev_b32_e32 v3, 2, v3
	v_and_b32_e32 v4, 0x3c0, v4
	v_and_b32_e32 v3, 32, v3
	v_bitop3_b32 v155, v4, v3, v173 bitop3:0x36
	v_or_b32_e32 v3, v175, v143
	v_lshlrev_b32_e32 v4, 6, v3
	v_lshlrev_b32_e32 v3, 2, v3
	v_and_b32_e32 v4, 0x3c0, v4
	v_and_b32_e32 v3, 32, v3
	v_bitop3_b32 v158, v4, v3, v173 bitop3:0x36
	v_or_b32_e32 v3, v174, v143
	v_lshlrev_b32_e32 v4, 6, v3
	v_lshlrev_b32_e32 v3, 2, v3
	v_lshlrev_b32_e32 v156, 7, v176
	v_lshlrev_b32_e32 v159, 7, v175
	v_and_b32_e32 v4, 0x3c0, v4
	v_and_b32_e32 v3, 32, v3
	v_lshlrev_b32_e32 v162, 7, v174
	v_or_b32_e32 v147, 0x400, v1
	v_or_b32_e32 v148, 0x800, v1
	v_or_b32_e32 v149, 0xc00, v1
	v_or_b32_e32 v154, 0x400, v172
	v_or_b32_e32 v157, 0x400, v156
	v_or_b32_e32 v160, 0x400, v159
	v_bitop3_b32 v161, v4, v3, v173 bitop3:0x36
	v_or_b32_e32 v163, 0x400, v162
	s_mov_b64 s[4:5], 0
	s_branch .LBB5_9

.LBB5_11:
	ds_read_b128 v[180:183], v166
	ds_read_b128 v[184:187], v166 offset:1024
	ds_read_b128 v[188:191], v166 offset:2048
	ds_read_b128 v[192:195], v166 offset:3072
	s_add_i32 s20, s2, s19
	s_add_i32 s4, s20, 1
	s_ashr_i32 s5, s4, 31
	s_lshl_b64 s[4:5], s[4:5], 7
	s_add_u32 s4, s3, s4
	s_addc_u32 s5, s7, s5
	v_readfirstlane_b32 s21, v176
	v_lshl_add_u64 v[196:197], s[4:5], 0, v[138:139]
	s_mov_b32 m0, s21
	s_nop 0
	global_load_lds_dwordx4 v[196:197], off
	v_lshl_add_u64 v[196:197], s[4:5], 0, v[140:141]
	v_readfirstlane_b32 s4, v177
	s_mov_b32 m0, s4
	s_nop 0
	global_load_lds_dwordx4 v[196:197], off
	ds_read_b128 v[196:199], v172
	ds_read_b128 v[200:203], v172 offset:1024
	ds_read_b128 v[204:207], v173
	ds_read_b128 v[208:211], v173 offset:1024
	ds_read_b128 v[212:215], v174
	ds_read_b128 v[216:219], v174 offset:1024
	ds_read_b128 v[220:223], v175
	ds_read_b128 v[224:227], v175 offset:1024
	ds_read_b128 v[228:231], v165
	ds_read_b128 v[232:235], v165 offset:1024
	ds_read_b128 v[236:239], v165 offset:2048
	ds_read_b128 v[240:243], v165 offset:3072
	s_waitcnt lgkmcnt(0)
	s_barrier
	s_setprio 1
	v_mfma_f32_16x16x32_f16 v[114:117], v[180:183], v[196:199], v[114:117]
	v_mfma_f32_16x16x32_f16 v[126:129], v[188:191], v[196:199], v[126:129]
	v_mfma_f32_16x16x32_f16 v[122:125], v[180:183], v[204:207], v[122:125]
	v_mfma_f32_16x16x32_f16 v[118:121], v[188:191], v[204:207], v[118:121]
	v_mfma_f32_16x16x32_f16 v[110:113], v[180:183], v[212:215], v[110:113]
	v_mfma_f32_16x16x32_f16 v[106:109], v[188:191], v[212:215], v[106:109]
	v_mfma_f32_16x16x32_f16 v[102:105], v[180:183], v[220:223], v[102:105]
	v_mfma_f32_16x16x32_f16 v[98:101], v[188:191], v[220:223], v[98:101]
	v_mfma_f32_16x16x32_f16 v[114:117], v[184:187], v[200:203], v[114:117]
	v_mfma_f32_16x16x32_f16 v[126:129], v[192:195], v[200:203], v[126:129]
	v_mfma_f32_16x16x32_f16 v[122:125], v[184:187], v[208:211], v[122:125]
	v_mfma_f32_16x16x32_f16 v[118:121], v[192:195], v[208:211], v[118:121]
	v_mfma_f32_16x16x32_f16 v[110:113], v[184:187], v[216:219], v[110:113]
	v_mfma_f32_16x16x32_f16 v[106:109], v[192:195], v[216:219], v[106:109]
	v_mfma_f32_16x16x32_f16 v[102:105], v[184:187], v[224:227], v[102:105]
	v_mfma_f32_16x16x32_f16 v[98:101], v[192:195], v[224:227], v[98:101]
	v_mfma_f32_16x16x32_f16 v[94:97], v[228:231], v[196:199], v[94:97]
	v_mfma_f32_16x16x32_f16 v[90:93], v[236:239], v[196:199], v[90:93]
	v_mfma_f32_16x16x32_f16 v[86:89], v[228:231], v[204:207], v[86:89]
	v_mfma_f32_16x16x32_f16 v[82:85], v[236:239], v[204:207], v[82:85]
	v_mfma_f32_16x16x32_f16 v[78:81], v[228:231], v[212:215], v[78:81]
	v_mfma_f32_16x16x32_f16 v[74:77], v[236:239], v[212:215], v[74:77]
	v_mfma_f32_16x16x32_f16 v[70:73], v[228:231], v[220:223], v[70:73]
	v_mfma_f32_16x16x32_f16 v[66:69], v[236:239], v[220:223], v[66:69]
	v_mfma_f32_16x16x32_f16 v[94:97], v[232:235], v[200:203], v[94:97]
	v_mfma_f32_16x16x32_f16 v[90:93], v[240:243], v[200:203], v[90:93]
	v_mfma_f32_16x16x32_f16 v[86:89], v[232:235], v[208:211], v[86:89]
	v_mfma_f32_16x16x32_f16 v[82:85], v[240:243], v[208:211], v[82:85]
	v_mfma_f32_16x16x32_f16 v[78:81], v[232:235], v[216:219], v[78:81]
	v_mfma_f32_16x16x32_f16 v[74:77], v[240:243], v[216:219], v[74:77]
	v_mfma_f32_16x16x32_f16 v[70:73], v[232:235], v[224:227], v[70:73]
	v_mfma_f32_16x16x32_f16 v[66:69], v[240:243], v[224:227], v[66:69]
	s_setprio 0
	s_barrier
	ds_read_b128 v[196:199], v172 offset:16384
	ds_read_b128 v[200:203], v172 offset:17408
	ds_read_b128 v[204:207], v173 offset:16384
	ds_read_b128 v[208:211], v173 offset:17408
	ds_read_b128 v[212:215], v174 offset:16384
	ds_read_b128 v[216:219], v174 offset:17408
	ds_read_b128 v[220:223], v175 offset:16384
	ds_read_b128 v[224:227], v175 offset:17408
	s_add_i32 s4, s20, 2
	s_ashr_i32 s5, s4, 31
	s_add_i32 s19, s19, 2
	s_lshl_b64 s[4:5], s[4:5], 7
	s_add_u32 s22, s13, s4
	s_addc_u32 s23, s14, s5
	v_readfirstlane_b32 s21, v167
	v_lshl_add_u64 v[244:245], s[22:23], 0, v[134:135]
	s_mov_b32 m0, s21
	v_readfirstlane_b32 s21, v178
	global_load_lds_dwordx4 v[244:245], off
	v_lshl_add_u64 v[244:245], s[22:23], 0, v[136:137]
	s_mov_b32 m0, s21
	s_nop 0
	global_load_lds_dwordx4 v[244:245], off
	s_add_u32 s22, s15, s4
	s_addc_u32 s23, s16, s5
	v_readfirstlane_b32 s21, v146
	v_lshl_add_u64 v[244:245], s[22:23], 0, v[138:139]
	s_mov_b32 m0, s21
	v_readfirstlane_b32 s21, v179
	global_load_lds_dwordx4 v[244:245], off
	v_lshl_add_u64 v[244:245], s[22:23], 0, v[140:141]
	s_mov_b32 m0, s21
	s_nop 0
	global_load_lds_dwordx4 v[244:245], off
	s_add_u32 s22, s17, s4
	s_addc_u32 s23, s18, s5
	v_readfirstlane_b32 s21, v169
	v_add_u32_e32 v246, 0x2000, v169
	v_lshl_add_u64 v[244:245], s[22:23], 0, v[134:135]
	s_mov_b32 m0, s21
	v_readfirstlane_b32 s21, v246
	global_load_lds_dwordx4 v[244:245], off
	v_lshl_add_u64 v[244:245], s[22:23], 0, v[136:137]
	s_mov_b32 m0, s21
	s_nop 0
	global_load_lds_dwordx4 v[244:245], off
	s_waitcnt vmcnt(6)
	s_waitcnt lgkmcnt(0)
	s_barrier
	s_setprio 1
	v_mfma_f32_16x16x32_f16 v[62:65], v[180:183], v[196:199], v[62:65]
	v_mfma_f32_16x16x32_f16 v[58:61], v[188:191], v[196:199], v[58:61]
	v_mfma_f32_16x16x32_f16 v[54:57], v[180:183], v[204:207], v[54:57]
	v_mfma_f32_16x16x32_f16 v[50:53], v[188:191], v[204:207], v[50:53]
	v_mfma_f32_16x16x32_f16 v[46:49], v[180:183], v[212:215], v[46:49]
	v_mfma_f32_16x16x32_f16 v[42:45], v[188:191], v[212:215], v[42:45]
	v_mfma_f32_16x16x32_f16 v[38:41], v[180:183], v[220:223], v[38:41]
	v_mfma_f32_16x16x32_f16 v[34:37], v[188:191], v[220:223], v[34:37]
	v_mfma_f32_16x16x32_f16 v[62:65], v[184:187], v[200:203], v[62:65]
	v_mfma_f32_16x16x32_f16 v[58:61], v[192:195], v[200:203], v[58:61]
	v_mfma_f32_16x16x32_f16 v[54:57], v[184:187], v[208:211], v[54:57]
	v_mfma_f32_16x16x32_f16 v[50:53], v[192:195], v[208:211], v[50:53]
	v_mfma_f32_16x16x32_f16 v[46:49], v[184:187], v[216:219], v[46:49]
	v_mfma_f32_16x16x32_f16 v[42:45], v[192:195], v[216:219], v[42:45]
	v_mfma_f32_16x16x32_f16 v[38:41], v[184:187], v[224:227], v[38:41]
	v_mfma_f32_16x16x32_f16 v[34:37], v[192:195], v[224:227], v[34:37]
	v_mfma_f32_16x16x32_f16 v[30:33], v[228:231], v[196:199], v[30:33]
	v_mfma_f32_16x16x32_f16 v[26:29], v[236:239], v[196:199], v[26:29]
	v_mfma_f32_16x16x32_f16 v[22:25], v[228:231], v[204:207], v[22:25]
	v_mfma_f32_16x16x32_f16 v[18:21], v[236:239], v[204:207], v[18:21]
	v_mfma_f32_16x16x32_f16 v[14:17], v[228:231], v[212:215], v[14:17]
	v_mfma_f32_16x16x32_f16 v[10:13], v[236:239], v[212:215], v[10:13]
	v_mfma_f32_16x16x32_f16 v[6:9], v[228:231], v[220:223], v[6:9]
	v_mfma_f32_16x16x32_f16 v[2:5], v[236:239], v[220:223], v[2:5]
	v_mfma_f32_16x16x32_f16 v[30:33], v[232:235], v[200:203], v[30:33]
	v_mfma_f32_16x16x32_f16 v[26:29], v[240:243], v[200:203], v[26:29]
	v_mfma_f32_16x16x32_f16 v[22:25], v[232:235], v[208:211], v[22:25]
	v_mfma_f32_16x16x32_f16 v[18:21], v[240:243], v[208:211], v[18:21]
	v_mfma_f32_16x16x32_f16 v[14:17], v[232:235], v[216:219], v[14:17]
	v_mfma_f32_16x16x32_f16 v[10:13], v[240:243], v[216:219], v[10:13]
	v_mfma_f32_16x16x32_f16 v[6:9], v[232:235], v[224:227], v[6:9]
	v_mfma_f32_16x16x32_f16 v[2:5], v[240:243], v[224:227], v[2:5]
	s_setprio 0
	s_barrier
	v_add_u32_e32 v192, v152, v1
	ds_read_b128 v[180:183], v192
	ds_read_b128 v[184:187], v192 offset:1024
	ds_read_b128 v[188:191], v192 offset:2048
	ds_read_b128 v[192:195], v192 offset:3072
	s_add_u32 s4, s3, s4
	v_add_u32_e32 v230, 0x4000, v146
	s_addc_u32 s5, s7, s5
	v_readfirstlane_b32 s21, v230
	v_lshl_add_u64 v[228:229], s[4:5], 0, v[138:139]
	s_mov_b32 m0, s21
	v_add_u32_e32 v230, 0x6000, v146
	ds_read_b128 v[196:199], v172 offset:32768
	ds_read_b128 v[200:203], v172 offset:33792
	ds_read_b128 v[204:207], v173 offset:32768
	ds_read_b128 v[208:211], v173 offset:33792
	ds_read_b128 v[212:215], v174 offset:32768
	ds_read_b128 v[216:219], v174 offset:33792
	ds_read_b128 v[220:223], v175 offset:32768
	ds_read_b128 v[224:227], v175 offset:33792
	global_load_lds_dwordx4 v[228:229], off
	v_lshl_add_u64 v[228:229], s[4:5], 0, v[140:141]
	v_readfirstlane_b32 s4, v230
	s_mov_b32 m0, s4
	s_nop 0
	global_load_lds_dwordx4 v[228:229], off
	v_add_u32_e32 v240, v150, v1
	ds_read_b128 v[228:231], v240
	ds_read_b128 v[232:235], v240 offset:1024
	ds_read_b128 v[236:239], v240 offset:2048
	ds_read_b128 v[240:243], v240 offset:3072
	s_waitcnt lgkmcnt(0)
	s_barrier
	s_setprio 1
	v_mfma_f32_16x16x32_f16 v[114:117], v[180:183], v[196:199], v[114:117]
	v_mfma_f32_16x16x32_f16 v[126:129], v[188:191], v[196:199], v[126:129]
	v_mfma_f32_16x16x32_f16 v[122:125], v[180:183], v[204:207], v[122:125]
	v_mfma_f32_16x16x32_f16 v[118:121], v[188:191], v[204:207], v[118:121]
	v_mfma_f32_16x16x32_f16 v[110:113], v[180:183], v[212:215], v[110:113]
	v_mfma_f32_16x16x32_f16 v[106:109], v[188:191], v[212:215], v[106:109]
	v_mfma_f32_16x16x32_f16 v[102:105], v[180:183], v[220:223], v[102:105]
	v_mfma_f32_16x16x32_f16 v[98:101], v[188:191], v[220:223], v[98:101]
	v_mfma_f32_16x16x32_f16 v[114:117], v[184:187], v[200:203], v[114:117]
	v_mfma_f32_16x16x32_f16 v[126:129], v[192:195], v[200:203], v[126:129]
	v_mfma_f32_16x16x32_f16 v[122:125], v[184:187], v[208:211], v[122:125]
	v_mfma_f32_16x16x32_f16 v[118:121], v[192:195], v[208:211], v[118:121]
	v_mfma_f32_16x16x32_f16 v[110:113], v[184:187], v[216:219], v[110:113]
	v_mfma_f32_16x16x32_f16 v[106:109], v[192:195], v[216:219], v[106:109]
	v_mfma_f32_16x16x32_f16 v[102:105], v[184:187], v[224:227], v[102:105]
	v_mfma_f32_16x16x32_f16 v[98:101], v[192:195], v[224:227], v[98:101]
	v_mfma_f32_16x16x32_f16 v[94:97], v[228:231], v[196:199], v[94:97]
	v_mfma_f32_16x16x32_f16 v[90:93], v[236:239], v[196:199], v[90:93]
	v_mfma_f32_16x16x32_f16 v[86:89], v[228:231], v[204:207], v[86:89]
	v_mfma_f32_16x16x32_f16 v[82:85], v[236:239], v[204:207], v[82:85]
	v_mfma_f32_16x16x32_f16 v[78:81], v[228:231], v[212:215], v[78:81]
	v_mfma_f32_16x16x32_f16 v[74:77], v[236:239], v[212:215], v[74:77]
	v_mfma_f32_16x16x32_f16 v[70:73], v[228:231], v[220:223], v[70:73]
	v_mfma_f32_16x16x32_f16 v[66:69], v[236:239], v[220:223], v[66:69]
	v_mfma_f32_16x16x32_f16 v[94:97], v[232:235], v[200:203], v[94:97]
	v_mfma_f32_16x16x32_f16 v[90:93], v[240:243], v[200:203], v[90:93]
	v_mfma_f32_16x16x32_f16 v[86:89], v[232:235], v[208:211], v[86:89]
	v_mfma_f32_16x16x32_f16 v[82:85], v[240:243], v[208:211], v[82:85]
	v_mfma_f32_16x16x32_f16 v[78:81], v[232:235], v[216:219], v[78:81]
	v_mfma_f32_16x16x32_f16 v[74:77], v[240:243], v[216:219], v[74:77]
	v_mfma_f32_16x16x32_f16 v[70:73], v[232:235], v[224:227], v[70:73]
	v_mfma_f32_16x16x32_f16 v[66:69], v[240:243], v[224:227], v[66:69]
	s_setprio 0
	s_barrier
	ds_read_b128 v[196:199], v172 offset:49152
	ds_read_b128 v[200:203], v172 offset:50176
	ds_read_b128 v[204:207], v173 offset:49152
	ds_read_b128 v[208:211], v173 offset:50176
	ds_read_b128 v[212:215], v174 offset:49152
	ds_read_b128 v[216:219], v174 offset:50176
	ds_read_b128 v[220:223], v175 offset:49152
	ds_read_b128 v[224:227], v175 offset:50176
	s_add_i32 s4, s20, 3
	s_ashr_i32 s5, s4, 31
	s_lshl_b64 s[4:5], s[4:5], 7
	s_add_u32 s20, s13, s4
	s_addc_u32 s21, s14, s5
	v_readfirstlane_b32 s22, v170
	v_lshl_add_u64 v[244:245], s[20:21], 0, v[134:135]
	s_mov_b32 m0, s22
	v_add_u32_e32 v246, 0x2000, v170
	global_load_lds_dwordx4 v[244:245], off
	v_lshl_add_u64 v[244:245], s[20:21], 0, v[136:137]
	v_readfirstlane_b32 s20, v246
	s_mov_b32 m0, s20
	s_nop 0
	global_load_lds_dwordx4 v[244:245], off
	s_add_u32 s20, s15, s4
	v_add_u32_e32 v246, 0x8000, v146
	s_addc_u32 s21, s16, s5
	v_readfirstlane_b32 s22, v246
	v_lshl_add_u64 v[244:245], s[20:21], 0, v[138:139]
	s_mov_b32 m0, s22
	v_add_u32_e32 v246, 0xa000, v146
	global_load_lds_dwordx4 v[244:245], off
	v_lshl_add_u64 v[244:245], s[20:21], 0, v[140:141]
	v_readfirstlane_b32 s20, v246
	s_mov_b32 m0, s20
	s_nop 0
	global_load_lds_dwordx4 v[244:245], off
	s_add_u32 s4, s17, s4
	s_addc_u32 s5, s18, s5
	v_readfirstlane_b32 s20, v171
	v_lshl_add_u64 v[244:245], s[4:5], 0, v[134:135]
	s_mov_b32 m0, s20
	v_add_u32_e32 v246, 0x2000, v171
	global_load_lds_dwordx4 v[244:245], off
	v_lshl_add_u64 v[244:245], s[4:5], 0, v[136:137]
	v_readfirstlane_b32 s4, v246
	s_mov_b32 m0, s4
	s_nop 0
	global_load_lds_dwordx4 v[244:245], off
	s_waitcnt vmcnt(6)
	s_waitcnt lgkmcnt(0)
	s_barrier
	s_setprio 1
	v_mfma_f32_16x16x32_f16 v[62:65], v[180:183], v[196:199], v[62:65]
	v_mfma_f32_16x16x32_f16 v[58:61], v[188:191], v[196:199], v[58:61]
	v_mfma_f32_16x16x32_f16 v[54:57], v[180:183], v[204:207], v[54:57]
	v_mfma_f32_16x16x32_f16 v[50:53], v[188:191], v[204:207], v[50:53]
	v_mfma_f32_16x16x32_f16 v[46:49], v[180:183], v[212:215], v[46:49]
	v_mfma_f32_16x16x32_f16 v[42:45], v[188:191], v[212:215], v[42:45]
	v_mfma_f32_16x16x32_f16 v[38:41], v[180:183], v[220:223], v[38:41]
	v_mfma_f32_16x16x32_f16 v[34:37], v[188:191], v[220:223], v[34:37]
	v_mfma_f32_16x16x32_f16 v[62:65], v[184:187], v[200:203], v[62:65]
	v_mfma_f32_16x16x32_f16 v[58:61], v[192:195], v[200:203], v[58:61]
	v_mfma_f32_16x16x32_f16 v[54:57], v[184:187], v[208:211], v[54:57]
	v_mfma_f32_16x16x32_f16 v[50:53], v[192:195], v[208:211], v[50:53]
	v_mfma_f32_16x16x32_f16 v[46:49], v[184:187], v[216:219], v[46:49]
	v_mfma_f32_16x16x32_f16 v[42:45], v[192:195], v[216:219], v[42:45]
	v_mfma_f32_16x16x32_f16 v[38:41], v[184:187], v[224:227], v[38:41]
	v_mfma_f32_16x16x32_f16 v[34:37], v[192:195], v[224:227], v[34:37]
	v_mfma_f32_16x16x32_f16 v[30:33], v[228:231], v[196:199], v[30:33]
	v_mfma_f32_16x16x32_f16 v[26:29], v[236:239], v[196:199], v[26:29]
	v_mfma_f32_16x16x32_f16 v[22:25], v[228:231], v[204:207], v[22:25]
	v_mfma_f32_16x16x32_f16 v[18:21], v[236:239], v[204:207], v[18:21]
	v_mfma_f32_16x16x32_f16 v[14:17], v[228:231], v[212:215], v[14:17]
	v_mfma_f32_16x16x32_f16 v[10:13], v[236:239], v[212:215], v[10:13]
	v_mfma_f32_16x16x32_f16 v[6:9], v[228:231], v[220:223], v[6:9]
	v_mfma_f32_16x16x32_f16 v[2:5], v[236:239], v[220:223], v[2:5]
	v_mfma_f32_16x16x32_f16 v[30:33], v[232:235], v[200:203], v[30:33]
	v_mfma_f32_16x16x32_f16 v[26:29], v[240:243], v[200:203], v[26:29]
	v_mfma_f32_16x16x32_f16 v[22:25], v[232:235], v[208:211], v[22:25]
	v_mfma_f32_16x16x32_f16 v[18:21], v[240:243], v[208:211], v[18:21]
	v_mfma_f32_16x16x32_f16 v[14:17], v[232:235], v[216:219], v[14:17]
	v_mfma_f32_16x16x32_f16 v[10:13], v[240:243], v[216:219], v[10:13]
	v_mfma_f32_16x16x32_f16 v[6:9], v[232:235], v[224:227], v[6:9]
	v_mfma_f32_16x16x32_f16 v[2:5], v[240:243], v[224:227], v[2:5]
	s_setprio 0
	s_cmp_ge_i32 s19, s10
	s_barrier
	s_cbranch_scc0 .LBB5_11
	v_mov_b32_e32 v172, v168

.LBB5_15:
	s_or_b64 exec, exec, s[2:3]
	s_ashr_i32 s13, s12, 31
	s_lshl_b64 s[2:3], s[12:13], 24
	v_lshlrev_b32_e32 v129, 5, v144
	s_add_u32 s0, s0, s2
	v_or3_b32 v130, v129, v142, s8
	v_or3_b32 v132, v143, v145, s9
	s_addc_u32 s1, s1, s3
	v_ashrrev_i32_e32 v131, 31, v130
	v_ashrrev_i32_e32 v133, 31, v132
	v_lshl_add_u64 v[130:131], v[130:131], 1, s[0:1]
	v_cvt_pk_f16_f32 v127, v126, v127
	v_cvt_pk_f16_f32 v126, v124, v125
	v_cvt_pk_f16_f32 v124, v120, v121
	v_lshlrev_b64 v[120:121], 12, v[132:133]
	v_or_b32_e32 v128, s6, v143
	v_cvt_pk_f16_f32 v125, v122, v123
	v_lshl_add_u64 v[120:121], v[130:131], 0, v[120:121]
	v_add_u32_e32 v128, v145, v128
	global_store_dwordx4 v[120:121], v[124:127], off
	v_or_b32_e32 v122, 16, v132
	v_ashrrev_i32_e32 v123, 31, v122
	v_cvt_pk_f16_f32 v119, v118, v119
	v_cvt_pk_f16_f32 v118, v116, v117
	v_cvt_pk_f16_f32 v116, v112, v113
	v_lshlrev_b64 v[112:113], 12, v[122:123]
	v_cvt_pk_f16_f32 v117, v114, v115
	v_lshl_add_u64 v[112:113], v[130:131], 0, v[112:113]
	global_store_dwordx4 v[112:113], v[116:119], off
	v_or_b32_e32 v114, 32, v132
	v_ashrrev_i32_e32 v115, 31, v114
	v_cvt_pk_f16_f32 v111, v110, v111
	v_cvt_pk_f16_f32 v110, v108, v109
	v_cvt_pk_f16_f32 v108, v104, v105
	v_lshlrev_b64 v[104:105], 12, v[114:115]
	v_cvt_pk_f16_f32 v109, v106, v107
	v_lshl_add_u64 v[104:105], v[130:131], 0, v[104:105]
	global_store_dwordx4 v[104:105], v[108:111], off
	v_or_b32_e32 v106, 48, v132
	v_ashrrev_i32_e32 v107, 31, v106
	v_cvt_pk_f16_f32 v95, v94, v95
	v_cvt_pk_f16_f32 v94, v92, v93
	v_cvt_pk_f16_f32 v92, v84, v85
	v_lshlrev_b64 v[84:85], 12, v[106:107]
	v_cvt_pk_f16_f32 v93, v86, v87
	v_lshl_add_u64 v[106:107], v[130:131], 0, v[84:85]
	global_store_dwordx4 v[106:107], v[92:95], off
	v_cvt_pk_f16_f32 v87, v102, v103
	v_cvt_pk_f16_f32 v86, v100, v101
	v_cvt_pk_f16_f32 v85, v98, v99
	v_cvt_pk_f16_f32 v84, v96, v97
	global_store_dwordx4 v[120:121], v[84:87], off offset:256
	s_nop 1
	v_cvt_pk_f16_f32 v85, v90, v91
	v_cvt_pk_f16_f32 v84, v88, v89
	v_cvt_pk_f16_f32 v83, v82, v83
	v_cvt_pk_f16_f32 v82, v80, v81
	global_store_dwordx4 v[112:113], v[82:85], off offset:256
	v_cvt_pk_f16_f32 v75, v74, v75
	v_cvt_pk_f16_f32 v74, v72, v73
	v_cvt_pk_f16_f32 v73, v66, v67
	v_cvt_pk_f16_f32 v72, v64, v65
	global_store_dwordx4 v[104:105], v[72:75], off offset:256
	v_cvt_pk_f16_f32 v63, v62, v63
	v_cvt_pk_f16_f32 v62, v60, v61
	v_cvt_pk_f16_f32 v61, v58, v59
	v_cvt_pk_f16_f32 v60, v56, v57
	global_store_dwordx4 v[106:107], v[60:63], off offset:256
	v_ashrrev_i32_e32 v129, 31, v128
	s_nop 0
	v_lshlrev_b64 v[60:61], 12, v[128:129]
	v_cvt_pk_f16_f32 v59, v78, v79
	v_cvt_pk_f16_f32 v58, v76, v77
	v_cvt_pk_f16_f32 v57, v70, v71
	v_cvt_pk_f16_f32 v56, v68, v69
	v_lshl_add_u64 v[60:61], v[130:131], 0, v[60:61]
	global_store_dwordx4 v[60:61], v[56:59], off
	s_nop 1
	v_or_b32_e32 v56, 16, v128
	v_ashrrev_i32_e32 v57, 31, v56
	v_cvt_pk_f16_f32 v55, v54, v55
	v_cvt_pk_f16_f32 v54, v52, v53
	v_cvt_pk_f16_f32 v52, v48, v49
	v_lshlrev_b64 v[48:49], 12, v[56:57]
	v_cvt_pk_f16_f32 v53, v50, v51
	v_lshl_add_u64 v[48:49], v[130:131], 0, v[48:49]
	global_store_dwordx4 v[48:49], v[52:55], off
	v_or_b32_e32 v50, 32, v128
	v_ashrrev_i32_e32 v51, 31, v50
	v_cvt_pk_f16_f32 v47, v46, v47
	v_cvt_pk_f16_f32 v46, v44, v45
	v_cvt_pk_f16_f32 v44, v40, v41
	v_lshlrev_b64 v[40:41], 12, v[50:51]
	v_cvt_pk_f16_f32 v45, v42, v43
	v_lshl_add_u64 v[40:41], v[130:131], 0, v[40:41]
	global_store_dwordx4 v[40:41], v[44:47], off
	v_or_b32_e32 v42, 48, v128
	v_ashrrev_i32_e32 v43, 31, v42
	v_cvt_pk_f16_f32 v39, v38, v39
	v_cvt_pk_f16_f32 v38, v36, v37
	v_cvt_pk_f16_f32 v36, v32, v33
	v_lshlrev_b64 v[32:33], 12, v[42:43]
	v_cvt_pk_f16_f32 v37, v34, v35
	v_lshl_add_u64 v[32:33], v[130:131], 0, v[32:33]
	global_store_dwordx4 v[32:33], v[36:39], off
	v_cvt_pk_f16_f32 v31, v30, v31
	v_cvt_pk_f16_f32 v30, v28, v29
	v_cvt_pk_f16_f32 v29, v26, v27
	v_cvt_pk_f16_f32 v28, v24, v25
	global_store_dwordx4 v[60:61], v[28:31], off offset:256
	v_cvt_pk_f16_f32 v23, v22, v23
	v_cvt_pk_f16_f32 v22, v20, v21
	v_cvt_pk_f16_f32 v21, v18, v19
	v_cvt_pk_f16_f32 v20, v16, v17
	global_store_dwordx4 v[48:49], v[20:23], off offset:256
	v_cvt_pk_f16_f32 v15, v14, v15
	v_cvt_pk_f16_f32 v14, v12, v13
	v_cvt_pk_f16_f32 v13, v10, v11
	v_cvt_pk_f16_f32 v12, v8, v9
	global_store_dwordx4 v[40:41], v[12:15], off offset:256
	v_cvt_pk_f16_f32 v7, v6, v7
	v_cvt_pk_f16_f32 v6, v4, v5
	v_cvt_pk_f16_f32 v5, v2, v3
	v_cvt_pk_f16_f32 v4, v0, v1
	global_store_dwordx4 v[32:33], v[4:7], off offset:256
	s_endpgm
	.p2align	8

.LBB7_14:
	s_or_b64 exec, exec, s[0:1]
	v_or_b32_e32 v146, s23, v168
	v_ashrrev_i32_e32 v147, 31, v146
	v_lshl_add_u64 v[12:13], v[146:147], 2, s[12:13]
	global_load_dwordx4 v[52:55], v[12:13], off
	global_load_dwordx4 v[48:51], v[12:13], off offset:16
	global_load_dwordx4 v[8:11], v[12:13], off offset:528
	s_nop 0
	global_load_dwordx4 v[12:15], v[12:13], off offset:512
	s_mov_b32 s2, 0xc0135761
	s_mov_b32 s0, 0x3dd2d3e8
	v_mov_b64_e32 v[144:145], s[2:3]
	v_or_b32_e32 v148, s11, v167
	v_ashrrev_i32_e32 v149, 31, v148
	v_lshl_add_u64 v[146:147], v[146:147], 1, s[8:9]
	v_lshlrev_b64 v[150:151], 14, v[148:149]
	s_waitcnt vmcnt(0)
	v_pk_add_f32 v[138:139], v[138:139], v[54:55]
	v_pk_add_f32 v[136:137], v[136:137], v[52:53]
	v_pk_add_f32 v[142:143], v[142:143], v[50:51]
	v_pk_add_f32 v[140:141], v[140:141], v[48:49]
	v_pk_mul_f32 v[152:153], v[138:139], v[138:139]
	v_pk_mul_f32 v[154:155], v[136:137], v[136:137]
	v_pk_mul_f32 v[156:157], v[142:143], v[142:143]
	v_pk_mul_f32 v[158:159], v[140:141], v[140:141]
	v_pk_fma_f32 v[154:155], v[154:155], s[0:1], v[144:145] op_sel_hi:[1,0,0] neg_lo:[1,0,0] neg_hi:[1,0,0]
	v_pk_fma_f32 v[152:153], v[152:153], s[0:1], v[144:145] op_sel_hi:[1,0,0] neg_lo:[1,0,0] neg_hi:[1,0,0]
	v_pk_fma_f32 v[158:159], v[158:159], s[0:1], v[144:145] op_sel_hi:[1,0,0] neg_lo:[1,0,0] neg_hi:[1,0,0]
	v_pk_fma_f32 v[156:157], v[156:157], s[0:1], v[144:145] op_sel_hi:[1,0,0] neg_lo:[1,0,0] neg_hi:[1,0,0]
	v_pk_mul_f32 v[154:155], v[136:137], v[154:155]
	v_pk_mul_f32 v[152:153], v[138:139], v[152:153]
	v_pk_mul_f32 v[158:159], v[140:141], v[158:159]
	v_pk_mul_f32 v[156:157], v[142:143], v[156:157]
	v_exp_f32_e32 v154, v154
	v_exp_f32_e32 v155, v155
	v_exp_f32_e32 v152, v152
	v_exp_f32_e32 v153, v153
	v_exp_f32_e32 v158, v158
	v_exp_f32_e32 v159, v159
	v_exp_f32_e32 v156, v156
	v_exp_f32_e32 v157, v157
	v_pk_add_f32 v[154:155], v[154:155], 1.0 op_sel_hi:[1,0]
	v_pk_add_f32 v[152:153], v[152:153], 1.0 op_sel_hi:[1,0]
	v_pk_add_f32 v[158:159], v[158:159], 1.0 op_sel_hi:[1,0]
	v_pk_add_f32 v[156:157], v[156:157], 1.0 op_sel_hi:[1,0]
	v_rcp_f32_e32 v154, v154
	v_rcp_f32_e32 v155, v155
	v_rcp_f32_e32 v152, v152
	v_rcp_f32_e32 v153, v153
	v_rcp_f32_e32 v158, v158
	v_rcp_f32_e32 v159, v159
	v_rcp_f32_e32 v156, v156
	v_rcp_f32_e32 v157, v157
	v_pk_mul_f32 v[136:137], v[136:137], v[154:155]
	v_pk_mul_f32 v[138:139], v[138:139], v[152:153]
	v_pk_mul_f32 v[152:153], v[140:141], v[158:159]
	v_pk_mul_f32 v[140:141], v[142:143], v[156:157]
	v_cvt_pk_f16_f32 v139, v138, v139
	v_cvt_pk_f16_f32 v141, v140, v141
	v_cvt_pk_f16_f32 v140, v152, v153
	v_cvt_pk_f16_f32 v138, v136, v137
	v_lshl_add_u64 v[136:137], v[146:147], 0, v[150:151]
	global_store_dwordx4 v[136:137], v[138:141], off
	v_pk_add_f32 v[128:129], v[128:129], v[48:49]
	v_pk_add_f32 v[134:135], v[134:135], v[54:55]
	v_pk_add_f32 v[132:133], v[132:133], v[52:53]
	v_pk_add_f32 v[130:131], v[130:131], v[50:51]
	v_pk_mul_f32 v[152:153], v[128:129], v[128:129]
	v_pk_mul_f32 v[140:141], v[134:135], v[134:135]
	v_pk_mul_f32 v[142:143], v[132:133], v[132:133]
	v_pk_mul_f32 v[150:151], v[130:131], v[130:131]
	v_pk_fma_f32 v[152:153], v[152:153], s[0:1], v[144:145] op_sel_hi:[1,0,0] neg_lo:[1,0,0] neg_hi:[1,0,0]
	v_pk_fma_f32 v[142:143], v[142:143], s[0:1], v[144:145] op_sel_hi:[1,0,0] neg_lo:[1,0,0] neg_hi:[1,0,0]
	v_pk_fma_f32 v[140:141], v[140:141], s[0:1], v[144:145] op_sel_hi:[1,0,0] neg_lo:[1,0,0] neg_hi:[1,0,0]
	v_pk_mul_f32 v[152:153], v[128:129], v[152:153]
	v_pk_fma_f32 v[150:151], v[150:151], s[0:1], v[144:145] op_sel_hi:[1,0,0] neg_lo:[1,0,0] neg_hi:[1,0,0]
	v_pk_mul_f32 v[142:143], v[132:133], v[142:143]
	v_pk_mul_f32 v[140:141], v[134:135], v[140:141]
	v_exp_f32_e32 v152, v152
	v_exp_f32_e32 v153, v153
	v_pk_mul_f32 v[150:151], v[130:131], v[150:151]
	v_exp_f32_e32 v142, v142
	v_exp_f32_e32 v143, v143
	v_exp_f32_e32 v140, v140
	v_exp_f32_e32 v141, v141
	v_exp_f32_e32 v150, v150
	v_exp_f32_e32 v151, v151
	v_pk_add_f32 v[152:153], v[152:153], 1.0 op_sel_hi:[1,0]
	v_pk_add_f32 v[142:143], v[142:143], 1.0 op_sel_hi:[1,0]
	v_pk_add_f32 v[140:141], v[140:141], 1.0 op_sel_hi:[1,0]
	v_rcp_f32_e32 v152, v152
	v_rcp_f32_e32 v153, v153
	v_pk_add_f32 v[150:151], v[150:151], 1.0 op_sel_hi:[1,0]
	v_rcp_f32_e32 v142, v142
	v_rcp_f32_e32 v143, v143
	v_rcp_f32_e32 v140, v140
	v_rcp_f32_e32 v141, v141
	v_rcp_f32_e32 v150, v150
	v_rcp_f32_e32 v151, v151
	v_or_b32_e32 v138, 16, v148
	v_pk_mul_f32 v[128:129], v[128:129], v[152:153]
	v_ashrrev_i32_e32 v139, 31, v138
	v_pk_mul_f32 v[142:143], v[132:133], v[142:143]
	v_pk_mul_f32 v[134:135], v[134:135], v[140:141]
	v_pk_mul_f32 v[130:131], v[130:131], v[150:151]
	v_cvt_pk_f16_f32 v132, v128, v129
	v_lshlrev_b64 v[128:129], 14, v[138:139]
	v_cvt_pk_f16_f32 v133, v130, v131
	v_cvt_pk_f16_f32 v131, v134, v135
	v_cvt_pk_f16_f32 v130, v142, v143
	v_lshl_add_u64 v[128:129], v[146:147], 0, v[128:129]
	global_store_dwordx4 v[128:129], v[130:133], off
	v_pk_add_f32 v[120:121], v[120:121], v[48:49]
	v_pk_add_f32 v[126:127], v[126:127], v[54:55]
	v_pk_add_f32 v[124:125], v[124:125], v[52:53]
	v_pk_add_f32 v[122:123], v[122:123], v[50:51]
	v_pk_mul_f32 v[140:141], v[120:121], v[120:121]
	v_pk_mul_f32 v[132:133], v[126:127], v[126:127]
	v_pk_mul_f32 v[134:135], v[124:125], v[124:125]
	v_pk_mul_f32 v[138:139], v[122:123], v[122:123]
	v_pk_fma_f32 v[140:141], v[140:141], s[0:1], v[144:145] op_sel_hi:[1,0,0] neg_lo:[1,0,0] neg_hi:[1,0,0]
	v_pk_fma_f32 v[134:135], v[134:135], s[0:1], v[144:145] op_sel_hi:[1,0,0] neg_lo:[1,0,0] neg_hi:[1,0,0]
	v_pk_fma_f32 v[132:133], v[132:133], s[0:1], v[144:145] op_sel_hi:[1,0,0] neg_lo:[1,0,0] neg_hi:[1,0,0]
	v_pk_mul_f32 v[140:141], v[120:121], v[140:141]
	v_pk_fma_f32 v[138:139], v[138:139], s[0:1], v[144:145] op_sel_hi:[1,0,0] neg_lo:[1,0,0] neg_hi:[1,0,0]
	v_pk_mul_f32 v[134:135], v[124:125], v[134:135]
	v_pk_mul_f32 v[132:133], v[126:127], v[132:133]
	v_exp_f32_e32 v140, v140
	v_exp_f32_e32 v141, v141
	v_pk_mul_f32 v[138:139], v[122:123], v[138:139]
	v_exp_f32_e32 v134, v134
	v_exp_f32_e32 v135, v135
	v_exp_f32_e32 v132, v132
	v_exp_f32_e32 v133, v133
	v_exp_f32_e32 v138, v138
	v_exp_f32_e32 v139, v139
	v_pk_add_f32 v[140:141], v[140:141], 1.0 op_sel_hi:[1,0]
	v_pk_add_f32 v[134:135], v[134:135], 1.0 op_sel_hi:[1,0]
	v_pk_add_f32 v[132:133], v[132:133], 1.0 op_sel_hi:[1,0]
	v_rcp_f32_e32 v140, v140
	v_rcp_f32_e32 v141, v141
	v_pk_add_f32 v[138:139], v[138:139], 1.0 op_sel_hi:[1,0]
	v_rcp_f32_e32 v134, v134
	v_rcp_f32_e32 v135, v135
	v_rcp_f32_e32 v132, v132
	v_rcp_f32_e32 v133, v133
	v_rcp_f32_e32 v138, v138
	v_rcp_f32_e32 v139, v139
	v_or_b32_e32 v130, 32, v148
	v_pk_mul_f32 v[120:121], v[120:121], v[140:141]
	v_ashrrev_i32_e32 v131, 31, v130
	v_pk_mul_f32 v[134:135], v[124:125], v[134:135]
	v_pk_mul_f32 v[126:127], v[126:127], v[132:133]
	v_pk_mul_f32 v[122:123], v[122:123], v[138:139]
	v_cvt_pk_f16_f32 v124, v120, v121
	v_lshlrev_b64 v[120:121], 14, v[130:131]
	v_cvt_pk_f16_f32 v125, v122, v123
	v_cvt_pk_f16_f32 v123, v126, v127
	v_cvt_pk_f16_f32 v122, v134, v135
	v_lshl_add_u64 v[120:121], v[146:147], 0, v[120:121]
	global_store_dwordx4 v[120:121], v[122:125], off
	v_pk_add_f32 v[112:113], v[112:113], v[48:49]
	v_pk_add_f32 v[118:119], v[118:119], v[54:55]
	v_pk_add_f32 v[116:117], v[116:117], v[52:53]
	v_pk_add_f32 v[114:115], v[114:115], v[50:51]
	v_pk_mul_f32 v[132:133], v[112:113], v[112:113]
	v_pk_mul_f32 v[124:125], v[118:119], v[118:119]
	v_pk_mul_f32 v[126:127], v[116:117], v[116:117]
	v_pk_mul_f32 v[130:131], v[114:115], v[114:115]
	v_pk_fma_f32 v[132:133], v[132:133], s[0:1], v[144:145] op_sel_hi:[1,0,0] neg_lo:[1,0,0] neg_hi:[1,0,0]
	v_pk_fma_f32 v[126:127], v[126:127], s[0:1], v[144:145] op_sel_hi:[1,0,0] neg_lo:[1,0,0] neg_hi:[1,0,0]
	v_pk_fma_f32 v[124:125], v[124:125], s[0:1], v[144:145] op_sel_hi:[1,0,0] neg_lo:[1,0,0] neg_hi:[1,0,0]
	v_pk_mul_f32 v[132:133], v[112:113], v[132:133]
	v_pk_fma_f32 v[130:131], v[130:131], s[0:1], v[144:145] op_sel_hi:[1,0,0] neg_lo:[1,0,0] neg_hi:[1,0,0]
	v_pk_mul_f32 v[126:127], v[116:117], v[126:127]
	v_pk_mul_f32 v[124:125], v[118:119], v[124:125]
	v_exp_f32_e32 v132, v132
	v_exp_f32_e32 v133, v133
	v_pk_mul_f32 v[130:131], v[114:115], v[130:131]
	v_exp_f32_e32 v126, v126
	v_exp_f32_e32 v127, v127
	v_exp_f32_e32 v124, v124
	v_exp_f32_e32 v125, v125
	v_exp_f32_e32 v130, v130
	v_exp_f32_e32 v131, v131
	v_pk_add_f32 v[132:133], v[132:133], 1.0 op_sel_hi:[1,0]
	v_pk_add_f32 v[126:127], v[126:127], 1.0 op_sel_hi:[1,0]
	v_pk_add_f32 v[124:125], v[124:125], 1.0 op_sel_hi:[1,0]
	v_rcp_f32_e32 v132, v132
	v_rcp_f32_e32 v133, v133
	v_pk_add_f32 v[130:131], v[130:131], 1.0 op_sel_hi:[1,0]
	v_rcp_f32_e32 v126, v126
	v_rcp_f32_e32 v127, v127
	v_rcp_f32_e32 v124, v124
	v_rcp_f32_e32 v125, v125
	v_rcp_f32_e32 v130, v130
	v_rcp_f32_e32 v131, v131
	v_or_b32_e32 v122, 48, v148
	v_pk_mul_f32 v[112:113], v[112:113], v[132:133]
	v_ashrrev_i32_e32 v123, 31, v122
	v_pk_mul_f32 v[126:127], v[116:117], v[126:127]
	v_pk_mul_f32 v[118:119], v[118:119], v[124:125]
	v_pk_mul_f32 v[114:115], v[114:115], v[130:131]
	v_cvt_pk_f16_f32 v116, v112, v113
	v_lshlrev_b64 v[112:113], 14, v[122:123]
	v_cvt_pk_f16_f32 v117, v114, v115
	v_cvt_pk_f16_f32 v115, v118, v119
	v_cvt_pk_f16_f32 v114, v126, v127
	v_lshl_add_u64 v[112:113], v[146:147], 0, v[112:113]
	global_store_dwordx4 v[112:113], v[114:117], off
	v_pk_add_f32 v[110:111], v[110:111], v[14:15]
	v_pk_add_f32 v[108:109], v[108:109], v[12:13]
	v_pk_add_f32 v[106:107], v[106:107], v[10:11]
	v_pk_add_f32 v[104:105], v[104:105], v[8:9]
	v_pk_mul_f32 v[114:115], v[110:111], v[110:111]
	v_pk_mul_f32 v[116:117], v[108:109], v[108:109]
	v_pk_mul_f32 v[118:119], v[106:107], v[106:107]
	v_pk_mul_f32 v[122:123], v[104:105], v[104:105]
	v_pk_fma_f32 v[116:117], v[116:117], s[0:1], v[144:145] op_sel_hi:[1,0,0] neg_lo:[1,0,0] neg_hi:[1,0,0]
	v_pk_fma_f32 v[114:115], v[114:115], s[0:1], v[144:145] op_sel_hi:[1,0,0] neg_lo:[1,0,0] neg_hi:[1,0,0]
	v_pk_fma_f32 v[122:123], v[122:123], s[0:1], v[144:145] op_sel_hi:[1,0,0] neg_lo:[1,0,0] neg_hi:[1,0,0]
	v_pk_fma_f32 v[118:119], v[118:119], s[0:1], v[144:145] op_sel_hi:[1,0,0] neg_lo:[1,0,0] neg_hi:[1,0,0]
	v_pk_mul_f32 v[116:117], v[108:109], v[116:117]
	v_pk_mul_f32 v[114:115], v[110:111], v[114:115]
	v_pk_mul_f32 v[122:123], v[104:105], v[122:123]
	v_pk_mul_f32 v[118:119], v[106:107], v[118:119]
	v_exp_f32_e32 v116, v116
	v_exp_f32_e32 v117, v117
	v_exp_f32_e32 v114, v114
	v_exp_f32_e32 v115, v115
	v_exp_f32_e32 v122, v122
	v_exp_f32_e32 v123, v123
	v_exp_f32_e32 v118, v118
	v_exp_f32_e32 v119, v119
	v_pk_add_f32 v[116:117], v[116:117], 1.0 op_sel_hi:[1,0]
	v_pk_add_f32 v[114:115], v[114:115], 1.0 op_sel_hi:[1,0]
	v_pk_add_f32 v[122:123], v[122:123], 1.0 op_sel_hi:[1,0]
	v_pk_add_f32 v[118:119], v[118:119], 1.0 op_sel_hi:[1,0]
	v_rcp_f32_e32 v116, v116
	v_rcp_f32_e32 v117, v117
	v_rcp_f32_e32 v114, v114
	v_rcp_f32_e32 v115, v115
	v_rcp_f32_e32 v122, v122
	v_rcp_f32_e32 v123, v123
	v_rcp_f32_e32 v118, v118
	v_rcp_f32_e32 v119, v119
	v_pk_mul_f32 v[108:109], v[108:109], v[116:117]
	v_pk_mul_f32 v[110:111], v[110:111], v[114:115]
	v_pk_mul_f32 v[114:115], v[104:105], v[122:123]
	v_pk_mul_f32 v[104:105], v[106:107], v[118:119]
	v_cvt_pk_f16_f32 v106, v114, v115
	v_cvt_pk_f16_f32 v107, v104, v105
	v_cvt_pk_f16_f32 v105, v110, v111
	v_cvt_pk_f16_f32 v104, v108, v109
	global_store_dwordx4 v[136:137], v[104:107], off offset:256
	v_pk_add_f32 v[102:103], v[102:103], v[14:15]
	v_pk_add_f32 v[100:101], v[100:101], v[12:13]
	v_pk_add_f32 v[98:99], v[98:99], v[10:11]
	v_pk_add_f32 v[96:97], v[96:97], v[8:9]
	v_pk_mul_f32 v[104:105], v[102:103], v[102:103]
	v_pk_mul_f32 v[106:107], v[100:101], v[100:101]
	v_pk_mul_f32 v[108:109], v[98:99], v[98:99]
	v_pk_mul_f32 v[110:111], v[96:97], v[96:97]
	v_pk_fma_f32 v[106:107], v[106:107], s[0:1], v[144:145] op_sel_hi:[1,0,0] neg_lo:[1,0,0] neg_hi:[1,0,0]
	v_pk_fma_f32 v[104:105], v[104:105], s[0:1], v[144:145] op_sel_hi:[1,0,0] neg_lo:[1,0,0] neg_hi:[1,0,0]
	v_pk_fma_f32 v[110:111], v[110:111], s[0:1], v[144:145] op_sel_hi:[1,0,0] neg_lo:[1,0,0] neg_hi:[1,0,0]
	v_pk_fma_f32 v[108:109], v[108:109], s[0:1], v[144:145] op_sel_hi:[1,0,0] neg_lo:[1,0,0] neg_hi:[1,0,0]
	v_pk_mul_f32 v[106:107], v[100:101], v[106:107]
	v_pk_mul_f32 v[104:105], v[102:103], v[104:105]
	v_pk_mul_f32 v[110:111], v[96:97], v[110:111]
	v_pk_mul_f32 v[108:109], v[98:99], v[108:109]
	v_exp_f32_e32 v106, v106
	v_exp_f32_e32 v107, v107
	v_exp_f32_e32 v104, v104
	v_exp_f32_e32 v105, v105
	v_exp_f32_e32 v110, v110
	v_exp_f32_e32 v111, v111
	v_exp_f32_e32 v108, v108
	v_exp_f32_e32 v109, v109
	v_pk_add_f32 v[106:107], v[106:107], 1.0 op_sel_hi:[1,0]
	v_pk_add_f32 v[104:105], v[104:105], 1.0 op_sel_hi:[1,0]
	v_pk_add_f32 v[110:111], v[110:111], 1.0 op_sel_hi:[1,0]
	v_pk_add_f32 v[108:109], v[108:109], 1.0 op_sel_hi:[1,0]
	v_rcp_f32_e32 v106, v106
	v_rcp_f32_e32 v107, v107
	v_rcp_f32_e32 v104, v104
	v_rcp_f32_e32 v105, v105
	v_rcp_f32_e32 v110, v110
	v_rcp_f32_e32 v111, v111
	v_rcp_f32_e32 v108, v108
	v_rcp_f32_e32 v109, v109
	v_pk_mul_f32 v[100:101], v[100:101], v[106:107]
	v_pk_mul_f32 v[102:103], v[102:103], v[104:105]
	v_pk_mul_f32 v[104:105], v[96:97], v[110:111]
	v_pk_mul_f32 v[96:97], v[98:99], v[108:109]
	v_cvt_pk_f16_f32 v98, v104, v105
	v_cvt_pk_f16_f32 v99, v96, v97
	v_cvt_pk_f16_f32 v97, v102, v103
	v_cvt_pk_f16_f32 v96, v100, v101
	global_store_dwordx4 v[128:129], v[96:99], off offset:256
	v_pk_add_f32 v[94:95], v[94:95], v[14:15]
	v_pk_add_f32 v[92:93], v[92:93], v[12:13]
	v_pk_add_f32 v[90:91], v[90:91], v[10:11]
	v_pk_add_f32 v[88:89], v[88:89], v[8:9]
	v_pk_mul_f32 v[96:97], v[94:95], v[94:95]
	v_pk_mul_f32 v[98:99], v[92:93], v[92:93]
	v_pk_mul_f32 v[100:101], v[90:91], v[90:91]
	v_pk_mul_f32 v[102:103], v[88:89], v[88:89]
	v_pk_fma_f32 v[98:99], v[98:99], s[0:1], v[144:145] op_sel_hi:[1,0,0] neg_lo:[1,0,0] neg_hi:[1,0,0]
	v_pk_fma_f32 v[96:97], v[96:97], s[0:1], v[144:145] op_sel_hi:[1,0,0] neg_lo:[1,0,0] neg_hi:[1,0,0]
	v_pk_fma_f32 v[102:103], v[102:103], s[0:1], v[144:145] op_sel_hi:[1,0,0] neg_lo:[1,0,0] neg_hi:[1,0,0]
	v_pk_fma_f32 v[100:101], v[100:101], s[0:1], v[144:145] op_sel_hi:[1,0,0] neg_lo:[1,0,0] neg_hi:[1,0,0]
	v_pk_mul_f32 v[98:99], v[92:93], v[98:99]
	v_pk_mul_f32 v[96:97], v[94:95], v[96:97]
	v_pk_mul_f32 v[102:103], v[88:89], v[102:103]
	v_pk_mul_f32 v[100:101], v[90:91], v[100:101]
	v_exp_f32_e32 v98, v98
	v_exp_f32_e32 v99, v99
	v_exp_f32_e32 v96, v96
	v_exp_f32_e32 v97, v97
	v_exp_f32_e32 v102, v102
	v_exp_f32_e32 v103, v103
	v_exp_f32_e32 v100, v100
	v_exp_f32_e32 v101, v101
	v_pk_add_f32 v[98:99], v[98:99], 1.0 op_sel_hi:[1,0]
	v_pk_add_f32 v[96:97], v[96:97], 1.0 op_sel_hi:[1,0]
	v_pk_add_f32 v[102:103], v[102:103], 1.0 op_sel_hi:[1,0]
	v_pk_add_f32 v[100:101], v[100:101], 1.0 op_sel_hi:[1,0]
	v_rcp_f32_e32 v98, v98
	v_rcp_f32_e32 v99, v99
	v_rcp_f32_e32 v96, v96
	v_rcp_f32_e32 v97, v97
	v_rcp_f32_e32 v102, v102
	v_rcp_f32_e32 v103, v103
	v_rcp_f32_e32 v100, v100
	v_rcp_f32_e32 v101, v101
	v_pk_mul_f32 v[92:93], v[92:93], v[98:99]
	v_pk_mul_f32 v[94:95], v[94:95], v[96:97]
	v_pk_mul_f32 v[96:97], v[88:89], v[102:103]
	v_pk_mul_f32 v[88:89], v[90:91], v[100:101]
	v_cvt_pk_f16_f32 v90, v96, v97
	v_cvt_pk_f16_f32 v91, v88, v89
	v_cvt_pk_f16_f32 v89, v94, v95
	v_cvt_pk_f16_f32 v88, v92, v93
	global_store_dwordx4 v[120:121], v[88:91], off offset:256
	v_pk_add_f32 v[86:87], v[86:87], v[14:15]
	v_pk_add_f32 v[84:85], v[84:85], v[12:13]
	v_pk_add_f32 v[82:83], v[82:83], v[10:11]
	v_pk_add_f32 v[80:81], v[80:81], v[8:9]
	v_pk_mul_f32 v[88:89], v[86:87], v[86:87]
	v_pk_mul_f32 v[90:91], v[84:85], v[84:85]
	v_pk_mul_f32 v[92:93], v[82:83], v[82:83]
	v_pk_mul_f32 v[94:95], v[80:81], v[80:81]
	v_pk_fma_f32 v[90:91], v[90:91], s[0:1], v[144:145] op_sel_hi:[1,0,0] neg_lo:[1,0,0] neg_hi:[1,0,0]
	v_pk_fma_f32 v[88:89], v[88:89], s[0:1], v[144:145] op_sel_hi:[1,0,0] neg_lo:[1,0,0] neg_hi:[1,0,0]
	v_pk_fma_f32 v[94:95], v[94:95], s[0:1], v[144:145] op_sel_hi:[1,0,0] neg_lo:[1,0,0] neg_hi:[1,0,0]
	v_pk_fma_f32 v[92:93], v[92:93], s[0:1], v[144:145] op_sel_hi:[1,0,0] neg_lo:[1,0,0] neg_hi:[1,0,0]
	v_pk_mul_f32 v[90:91], v[84:85], v[90:91]
	v_pk_mul_f32 v[88:89], v[86:87], v[88:89]
	v_pk_mul_f32 v[94:95], v[80:81], v[94:95]
	v_pk_mul_f32 v[92:93], v[82:83], v[92:93]
	v_exp_f32_e32 v90, v90
	v_exp_f32_e32 v91, v91
	v_exp_f32_e32 v88, v88
	v_exp_f32_e32 v89, v89
	v_exp_f32_e32 v94, v94
	v_exp_f32_e32 v95, v95
	v_exp_f32_e32 v92, v92
	v_exp_f32_e32 v93, v93
	v_pk_add_f32 v[90:91], v[90:91], 1.0 op_sel_hi:[1,0]
	v_pk_add_f32 v[88:89], v[88:89], 1.0 op_sel_hi:[1,0]
	v_pk_add_f32 v[94:95], v[94:95], 1.0 op_sel_hi:[1,0]
	v_pk_add_f32 v[92:93], v[92:93], 1.0 op_sel_hi:[1,0]
	v_rcp_f32_e32 v90, v90
	v_rcp_f32_e32 v91, v91
	v_rcp_f32_e32 v88, v88
	v_rcp_f32_e32 v89, v89
	v_rcp_f32_e32 v94, v94
	v_rcp_f32_e32 v95, v95
	v_rcp_f32_e32 v92, v92
	v_rcp_f32_e32 v93, v93
	v_pk_mul_f32 v[84:85], v[84:85], v[90:91]
	v_pk_mul_f32 v[86:87], v[86:87], v[88:89]
	v_pk_mul_f32 v[88:89], v[80:81], v[94:95]
	v_pk_mul_f32 v[80:81], v[82:83], v[92:93]
	v_cvt_pk_f16_f32 v82, v88, v89
	v_cvt_pk_f16_f32 v83, v80, v81
	v_cvt_pk_f16_f32 v81, v86, v87
	v_cvt_pk_f16_f32 v80, v84, v85
	global_store_dwordx4 v[112:113], v[80:83], off offset:256
	v_pk_add_f32 v[72:73], v[72:73], v[48:49]
	v_pk_add_f32 v[78:79], v[78:79], v[54:55]
	v_pk_add_f32 v[76:77], v[76:77], v[52:53]
	v_pk_add_f32 v[74:75], v[74:75], v[50:51]
	v_pk_mul_f32 v[88:89], v[72:73], v[72:73]
	v_pk_mul_f32 v[82:83], v[78:79], v[78:79]
	v_pk_mul_f32 v[84:85], v[76:77], v[76:77]
	v_pk_mul_f32 v[86:87], v[74:75], v[74:75]
	v_pk_fma_f32 v[88:89], v[88:89], s[0:1], v[144:145] op_sel_hi:[1,0,0] neg_lo:[1,0,0] neg_hi:[1,0,0]
	v_pk_fma_f32 v[84:85], v[84:85], s[0:1], v[144:145] op_sel_hi:[1,0,0] neg_lo:[1,0,0] neg_hi:[1,0,0]
	v_pk_fma_f32 v[82:83], v[82:83], s[0:1], v[144:145] op_sel_hi:[1,0,0] neg_lo:[1,0,0] neg_hi:[1,0,0]
	v_pk_mul_f32 v[88:89], v[72:73], v[88:89]
	v_pk_fma_f32 v[86:87], v[86:87], s[0:1], v[144:145] op_sel_hi:[1,0,0] neg_lo:[1,0,0] neg_hi:[1,0,0]
	v_pk_mul_f32 v[84:85], v[76:77], v[84:85]
	v_pk_mul_f32 v[82:83], v[78:79], v[82:83]
	v_exp_f32_e32 v88, v88
	v_exp_f32_e32 v89, v89
	v_pk_mul_f32 v[86:87], v[74:75], v[86:87]
	v_exp_f32_e32 v84, v84
	v_exp_f32_e32 v85, v85
	v_exp_f32_e32 v82, v82
	v_exp_f32_e32 v83, v83
	v_exp_f32_e32 v86, v86
	v_exp_f32_e32 v87, v87
	v_pk_add_f32 v[88:89], v[88:89], 1.0 op_sel_hi:[1,0]
	v_pk_add_f32 v[84:85], v[84:85], 1.0 op_sel_hi:[1,0]
	v_pk_add_f32 v[82:83], v[82:83], 1.0 op_sel_hi:[1,0]
	v_rcp_f32_e32 v88, v88
	v_rcp_f32_e32 v89, v89
	v_pk_add_f32 v[86:87], v[86:87], 1.0 op_sel_hi:[1,0]
	v_rcp_f32_e32 v84, v84
	v_rcp_f32_e32 v85, v85
	v_rcp_f32_e32 v82, v82
	v_rcp_f32_e32 v83, v83
	v_rcp_f32_e32 v86, v86
	v_rcp_f32_e32 v87, v87
	v_add_u32_e32 v80, s11, v166
	v_pk_mul_f32 v[72:73], v[72:73], v[88:89]
	v_ashrrev_i32_e32 v81, 31, v80
	v_pk_mul_f32 v[84:85], v[76:77], v[84:85]
	v_pk_mul_f32 v[78:79], v[78:79], v[82:83]
	v_pk_mul_f32 v[74:75], v[74:75], v[86:87]
	v_cvt_pk_f16_f32 v76, v72, v73
	v_lshlrev_b64 v[72:73], 14, v[80:81]
	v_cvt_pk_f16_f32 v77, v74, v75
	v_cvt_pk_f16_f32 v75, v78, v79
	v_cvt_pk_f16_f32 v74, v84, v85
	v_lshl_add_u64 v[72:73], v[146:147], 0, v[72:73]
	global_store_dwordx4 v[72:73], v[74:77], off
	v_pk_add_f32 v[64:65], v[64:65], v[48:49]
	v_pk_add_f32 v[70:71], v[70:71], v[54:55]
	v_pk_add_f32 v[68:69], v[68:69], v[52:53]
	v_pk_add_f32 v[66:67], v[66:67], v[50:51]
	v_pk_mul_f32 v[84:85], v[64:65], v[64:65]
	v_pk_mul_f32 v[76:77], v[70:71], v[70:71]
	v_pk_mul_f32 v[78:79], v[68:69], v[68:69]
	v_pk_mul_f32 v[82:83], v[66:67], v[66:67]
	v_pk_fma_f32 v[84:85], v[84:85], s[0:1], v[144:145] op_sel_hi:[1,0,0] neg_lo:[1,0,0] neg_hi:[1,0,0]
	v_pk_fma_f32 v[78:79], v[78:79], s[0:1], v[144:145] op_sel_hi:[1,0,0] neg_lo:[1,0,0] neg_hi:[1,0,0]
	v_pk_fma_f32 v[76:77], v[76:77], s[0:1], v[144:145] op_sel_hi:[1,0,0] neg_lo:[1,0,0] neg_hi:[1,0,0]
	v_pk_mul_f32 v[84:85], v[64:65], v[84:85]
	v_pk_fma_f32 v[82:83], v[82:83], s[0:1], v[144:145] op_sel_hi:[1,0,0] neg_lo:[1,0,0] neg_hi:[1,0,0]
	v_pk_mul_f32 v[78:79], v[68:69], v[78:79]
	v_pk_mul_f32 v[76:77], v[70:71], v[76:77]
	v_exp_f32_e32 v84, v84
	v_exp_f32_e32 v85, v85
	v_pk_mul_f32 v[82:83], v[66:67], v[82:83]
	v_exp_f32_e32 v78, v78
	v_exp_f32_e32 v79, v79
	v_exp_f32_e32 v76, v76
	v_exp_f32_e32 v77, v77
	v_exp_f32_e32 v82, v82
	v_exp_f32_e32 v83, v83
	v_pk_add_f32 v[84:85], v[84:85], 1.0 op_sel_hi:[1,0]
	v_pk_add_f32 v[78:79], v[78:79], 1.0 op_sel_hi:[1,0]
	v_pk_add_f32 v[76:77], v[76:77], 1.0 op_sel_hi:[1,0]
	v_rcp_f32_e32 v84, v84
	v_rcp_f32_e32 v85, v85
	v_pk_add_f32 v[82:83], v[82:83], 1.0 op_sel_hi:[1,0]
	v_rcp_f32_e32 v78, v78
	v_rcp_f32_e32 v79, v79
	v_rcp_f32_e32 v76, v76
	v_rcp_f32_e32 v77, v77
	v_rcp_f32_e32 v82, v82
	v_rcp_f32_e32 v83, v83
	v_or_b32_e32 v74, 16, v80
	v_pk_mul_f32 v[64:65], v[64:65], v[84:85]
	v_ashrrev_i32_e32 v75, 31, v74
	v_pk_mul_f32 v[78:79], v[68:69], v[78:79]
	v_pk_mul_f32 v[70:71], v[70:71], v[76:77]
	v_pk_mul_f32 v[66:67], v[66:67], v[82:83]
	v_cvt_pk_f16_f32 v68, v64, v65
	v_lshlrev_b64 v[64:65], 14, v[74:75]
	v_cvt_pk_f16_f32 v69, v66, v67
	v_cvt_pk_f16_f32 v67, v70, v71
	v_cvt_pk_f16_f32 v66, v78, v79
	v_lshl_add_u64 v[64:65], v[146:147], 0, v[64:65]
	global_store_dwordx4 v[64:65], v[66:69], off
	v_pk_add_f32 v[56:57], v[56:57], v[48:49]
	v_pk_add_f32 v[62:63], v[62:63], v[54:55]
	v_pk_add_f32 v[60:61], v[60:61], v[52:53]
	v_pk_add_f32 v[58:59], v[58:59], v[50:51]
	v_pk_mul_f32 v[76:77], v[56:57], v[56:57]
	v_pk_mul_f32 v[68:69], v[62:63], v[62:63]
	v_pk_mul_f32 v[70:71], v[60:61], v[60:61]
	v_pk_mul_f32 v[74:75], v[58:59], v[58:59]
	v_pk_fma_f32 v[76:77], v[76:77], s[0:1], v[144:145] op_sel_hi:[1,0,0] neg_lo:[1,0,0] neg_hi:[1,0,0]
	v_pk_fma_f32 v[70:71], v[70:71], s[0:1], v[144:145] op_sel_hi:[1,0,0] neg_lo:[1,0,0] neg_hi:[1,0,0]
	v_pk_fma_f32 v[68:69], v[68:69], s[0:1], v[144:145] op_sel_hi:[1,0,0] neg_lo:[1,0,0] neg_hi:[1,0,0]
	v_pk_mul_f32 v[76:77], v[56:57], v[76:77]
	v_pk_fma_f32 v[74:75], v[74:75], s[0:1], v[144:145] op_sel_hi:[1,0,0] neg_lo:[1,0,0] neg_hi:[1,0,0]
	v_pk_mul_f32 v[70:71], v[60:61], v[70:71]
	v_pk_mul_f32 v[68:69], v[62:63], v[68:69]
	v_exp_f32_e32 v76, v76
	v_exp_f32_e32 v77, v77
	v_pk_mul_f32 v[74:75], v[58:59], v[74:75]
	v_exp_f32_e32 v70, v70
	v_exp_f32_e32 v71, v71
	v_exp_f32_e32 v68, v68
	v_exp_f32_e32 v69, v69
	v_exp_f32_e32 v74, v74
	v_exp_f32_e32 v75, v75
	v_pk_add_f32 v[76:77], v[76:77], 1.0 op_sel_hi:[1,0]
	v_pk_add_f32 v[70:71], v[70:71], 1.0 op_sel_hi:[1,0]
	v_pk_add_f32 v[68:69], v[68:69], 1.0 op_sel_hi:[1,0]
	v_rcp_f32_e32 v76, v76
	v_rcp_f32_e32 v77, v77
	v_pk_add_f32 v[74:75], v[74:75], 1.0 op_sel_hi:[1,0]
	v_rcp_f32_e32 v70, v70
	v_rcp_f32_e32 v71, v71
	v_rcp_f32_e32 v68, v68
	v_rcp_f32_e32 v69, v69
	v_rcp_f32_e32 v74, v74
	v_rcp_f32_e32 v75, v75
	v_or_b32_e32 v66, 32, v80
	v_pk_mul_f32 v[56:57], v[56:57], v[76:77]
	v_ashrrev_i32_e32 v67, 31, v66
	v_pk_mul_f32 v[70:71], v[60:61], v[70:71]
	v_pk_mul_f32 v[62:63], v[62:63], v[68:69]
	v_pk_mul_f32 v[58:59], v[58:59], v[74:75]
	v_cvt_pk_f16_f32 v60, v56, v57
	v_lshlrev_b64 v[56:57], 14, v[66:67]
	v_cvt_pk_f16_f32 v61, v58, v59
	v_cvt_pk_f16_f32 v59, v62, v63
	v_cvt_pk_f16_f32 v58, v70, v71
	v_lshl_add_u64 v[56:57], v[146:147], 0, v[56:57]
	global_store_dwordx4 v[56:57], v[58:61], off
	v_pk_add_f32 v[40:41], v[40:41], v[48:49]
	v_pk_add_f32 v[46:47], v[46:47], v[54:55]
	v_pk_add_f32 v[44:45], v[44:45], v[52:53]
	v_pk_add_f32 v[42:43], v[42:43], v[50:51]
	v_pk_mul_f32 v[54:55], v[40:41], v[40:41]
	v_pk_mul_f32 v[48:49], v[46:47], v[46:47]
	v_pk_mul_f32 v[50:51], v[44:45], v[44:45]
	v_pk_mul_f32 v[52:53], v[42:43], v[42:43]
	v_pk_fma_f32 v[54:55], v[54:55], s[0:1], v[144:145] op_sel_hi:[1,0,0] neg_lo:[1,0,0] neg_hi:[1,0,0]
	v_pk_fma_f32 v[50:51], v[50:51], s[0:1], v[144:145] op_sel_hi:[1,0,0] neg_lo:[1,0,0] neg_hi:[1,0,0]
	v_pk_fma_f32 v[48:49], v[48:49], s[0:1], v[144:145] op_sel_hi:[1,0,0] neg_lo:[1,0,0] neg_hi:[1,0,0]
	v_pk_mul_f32 v[54:55], v[40:41], v[54:55]
	v_pk_fma_f32 v[52:53], v[52:53], s[0:1], v[144:145] op_sel_hi:[1,0,0] neg_lo:[1,0,0] neg_hi:[1,0,0]
	v_pk_mul_f32 v[50:51], v[44:45], v[50:51]
	v_pk_mul_f32 v[48:49], v[46:47], v[48:49]
	v_exp_f32_e32 v54, v54
	v_exp_f32_e32 v55, v55
	v_pk_mul_f32 v[52:53], v[42:43], v[52:53]
	v_exp_f32_e32 v50, v50
	v_exp_f32_e32 v51, v51
	v_exp_f32_e32 v48, v48
	v_exp_f32_e32 v49, v49
	v_exp_f32_e32 v52, v52
	v_exp_f32_e32 v53, v53
	v_pk_add_f32 v[54:55], v[54:55], 1.0 op_sel_hi:[1,0]
	v_pk_add_f32 v[50:51], v[50:51], 1.0 op_sel_hi:[1,0]
	v_pk_add_f32 v[48:49], v[48:49], 1.0 op_sel_hi:[1,0]
	v_rcp_f32_e32 v54, v54
	v_rcp_f32_e32 v55, v55
	v_pk_add_f32 v[52:53], v[52:53], 1.0 op_sel_hi:[1,0]
	v_rcp_f32_e32 v50, v50
	v_rcp_f32_e32 v51, v51
	v_rcp_f32_e32 v48, v48
	v_rcp_f32_e32 v49, v49
	v_rcp_f32_e32 v52, v52
	v_rcp_f32_e32 v53, v53
	v_or_b32_e32 v58, 48, v80
	v_pk_mul_f32 v[40:41], v[40:41], v[54:55]
	v_ashrrev_i32_e32 v59, 31, v58
	v_pk_mul_f32 v[50:51], v[44:45], v[50:51]
	v_pk_mul_f32 v[46:47], v[46:47], v[48:49]
	v_pk_mul_f32 v[42:43], v[42:43], v[52:53]
	v_cvt_pk_f16_f32 v44, v40, v41
	v_lshlrev_b64 v[40:41], 14, v[58:59]
	v_cvt_pk_f16_f32 v45, v42, v43
	v_cvt_pk_f16_f32 v43, v46, v47
	v_cvt_pk_f16_f32 v42, v50, v51
	v_lshl_add_u64 v[40:41], v[146:147], 0, v[40:41]
	global_store_dwordx4 v[40:41], v[42:45], off
	v_pk_add_f32 v[38:39], v[38:39], v[14:15]
	v_pk_add_f32 v[36:37], v[36:37], v[12:13]
	v_pk_add_f32 v[34:35], v[34:35], v[10:11]
	v_pk_add_f32 v[32:33], v[32:33], v[8:9]
	v_pk_mul_f32 v[42:43], v[38:39], v[38:39]
	v_pk_mul_f32 v[44:45], v[36:37], v[36:37]
	v_pk_mul_f32 v[46:47], v[34:35], v[34:35]
	v_pk_mul_f32 v[48:49], v[32:33], v[32:33]
	v_pk_fma_f32 v[44:45], v[44:45], s[0:1], v[144:145] op_sel_hi:[1,0,0] neg_lo:[1,0,0] neg_hi:[1,0,0]
	v_pk_fma_f32 v[42:43], v[42:43], s[0:1], v[144:145] op_sel_hi:[1,0,0] neg_lo:[1,0,0] neg_hi:[1,0,0]
	v_pk_fma_f32 v[48:49], v[48:49], s[0:1], v[144:145] op_sel_hi:[1,0,0] neg_lo:[1,0,0] neg_hi:[1,0,0]
	v_pk_fma_f32 v[46:47], v[46:47], s[0:1], v[144:145] op_sel_hi:[1,0,0] neg_lo:[1,0,0] neg_hi:[1,0,0]
	v_pk_mul_f32 v[44:45], v[36:37], v[44:45]
	v_pk_mul_f32 v[42:43], v[38:39], v[42:43]
	v_pk_mul_f32 v[48:49], v[32:33], v[48:49]
	v_pk_mul_f32 v[46:47], v[34:35], v[46:47]
	v_exp_f32_e32 v44, v44
	v_exp_f32_e32 v45, v45
	v_exp_f32_e32 v42, v42
	v_exp_f32_e32 v43, v43
	v_exp_f32_e32 v48, v48
	v_exp_f32_e32 v49, v49
	v_exp_f32_e32 v46, v46
	v_exp_f32_e32 v47, v47
	v_pk_add_f32 v[44:45], v[44:45], 1.0 op_sel_hi:[1,0]
	v_pk_add_f32 v[42:43], v[42:43], 1.0 op_sel_hi:[1,0]
	v_pk_add_f32 v[48:49], v[48:49], 1.0 op_sel_hi:[1,0]
	v_pk_add_f32 v[46:47], v[46:47], 1.0 op_sel_hi:[1,0]
	v_rcp_f32_e32 v44, v44
	v_rcp_f32_e32 v45, v45
	v_rcp_f32_e32 v42, v42
	v_rcp_f32_e32 v43, v43
	v_rcp_f32_e32 v48, v48
	v_rcp_f32_e32 v49, v49
	v_rcp_f32_e32 v46, v46
	v_rcp_f32_e32 v47, v47
	v_pk_mul_f32 v[36:37], v[36:37], v[44:45]
	v_pk_mul_f32 v[38:39], v[38:39], v[42:43]
	v_pk_mul_f32 v[42:43], v[32:33], v[48:49]
	v_pk_mul_f32 v[32:33], v[34:35], v[46:47]
	v_cvt_pk_f16_f32 v34, v42, v43
	v_cvt_pk_f16_f32 v35, v32, v33
	v_cvt_pk_f16_f32 v33, v38, v39
	v_cvt_pk_f16_f32 v32, v36, v37
	global_store_dwordx4 v[72:73], v[32:35], off offset:256
	v_pk_add_f32 v[30:31], v[30:31], v[14:15]
	v_pk_add_f32 v[28:29], v[28:29], v[12:13]
	v_pk_add_f32 v[26:27], v[26:27], v[10:11]
	v_pk_add_f32 v[24:25], v[24:25], v[8:9]
	v_pk_mul_f32 v[32:33], v[30:31], v[30:31]
	v_pk_mul_f32 v[34:35], v[28:29], v[28:29]
	v_pk_mul_f32 v[36:37], v[26:27], v[26:27]
	v_pk_mul_f32 v[38:39], v[24:25], v[24:25]
	v_pk_fma_f32 v[34:35], v[34:35], s[0:1], v[144:145] op_sel_hi:[1,0,0] neg_lo:[1,0,0] neg_hi:[1,0,0]
	v_pk_fma_f32 v[32:33], v[32:33], s[0:1], v[144:145] op_sel_hi:[1,0,0] neg_lo:[1,0,0] neg_hi:[1,0,0]
	v_pk_fma_f32 v[38:39], v[38:39], s[0:1], v[144:145] op_sel_hi:[1,0,0] neg_lo:[1,0,0] neg_hi:[1,0,0]
	v_pk_fma_f32 v[36:37], v[36:37], s[0:1], v[144:145] op_sel_hi:[1,0,0] neg_lo:[1,0,0] neg_hi:[1,0,0]
	v_pk_mul_f32 v[34:35], v[28:29], v[34:35]
	v_pk_mul_f32 v[32:33], v[30:31], v[32:33]
	v_pk_mul_f32 v[38:39], v[24:25], v[38:39]
	v_pk_mul_f32 v[36:37], v[26:27], v[36:37]
	v_exp_f32_e32 v34, v34
	v_exp_f32_e32 v35, v35
	v_exp_f32_e32 v32, v32
	v_exp_f32_e32 v33, v33
	v_exp_f32_e32 v38, v38
	v_exp_f32_e32 v39, v39
	v_exp_f32_e32 v36, v36
	v_exp_f32_e32 v37, v37
	v_pk_add_f32 v[34:35], v[34:35], 1.0 op_sel_hi:[1,0]
	v_pk_add_f32 v[32:33], v[32:33], 1.0 op_sel_hi:[1,0]
	v_pk_add_f32 v[38:39], v[38:39], 1.0 op_sel_hi:[1,0]
	v_pk_add_f32 v[36:37], v[36:37], 1.0 op_sel_hi:[1,0]
	v_rcp_f32_e32 v34, v34
	v_rcp_f32_e32 v35, v35
	v_rcp_f32_e32 v32, v32
	v_rcp_f32_e32 v33, v33
	v_rcp_f32_e32 v38, v38
	v_rcp_f32_e32 v39, v39
	v_rcp_f32_e32 v36, v36
	v_rcp_f32_e32 v37, v37
	v_pk_mul_f32 v[28:29], v[28:29], v[34:35]
	v_pk_mul_f32 v[30:31], v[30:31], v[32:33]
	v_pk_mul_f32 v[32:33], v[24:25], v[38:39]
	v_pk_mul_f32 v[24:25], v[26:27], v[36:37]
	v_cvt_pk_f16_f32 v26, v32, v33
	v_cvt_pk_f16_f32 v27, v24, v25
	v_cvt_pk_f16_f32 v25, v30, v31
	v_cvt_pk_f16_f32 v24, v28, v29
	global_store_dwordx4 v[64:65], v[24:27], off offset:256
	v_pk_add_f32 v[22:23], v[22:23], v[14:15]
	v_pk_add_f32 v[20:21], v[20:21], v[12:13]
	v_pk_add_f32 v[18:19], v[18:19], v[10:11]
	v_pk_add_f32 v[16:17], v[16:17], v[8:9]
	v_pk_mul_f32 v[24:25], v[22:23], v[22:23]
	v_pk_mul_f32 v[26:27], v[20:21], v[20:21]
	v_pk_mul_f32 v[28:29], v[18:19], v[18:19]
	v_pk_mul_f32 v[30:31], v[16:17], v[16:17]
	v_pk_fma_f32 v[26:27], v[26:27], s[0:1], v[144:145] op_sel_hi:[1,0,0] neg_lo:[1,0,0] neg_hi:[1,0,0]
	v_pk_fma_f32 v[24:25], v[24:25], s[0:1], v[144:145] op_sel_hi:[1,0,0] neg_lo:[1,0,0] neg_hi:[1,0,0]
	v_pk_fma_f32 v[30:31], v[30:31], s[0:1], v[144:145] op_sel_hi:[1,0,0] neg_lo:[1,0,0] neg_hi:[1,0,0]
	v_pk_fma_f32 v[28:29], v[28:29], s[0:1], v[144:145] op_sel_hi:[1,0,0] neg_lo:[1,0,0] neg_hi:[1,0,0]
	v_pk_mul_f32 v[26:27], v[20:21], v[26:27]
	v_pk_mul_f32 v[24:25], v[22:23], v[24:25]
	v_pk_mul_f32 v[30:31], v[16:17], v[30:31]
	v_pk_mul_f32 v[28:29], v[18:19], v[28:29]
	v_exp_f32_e32 v26, v26
	v_exp_f32_e32 v27, v27
	v_exp_f32_e32 v24, v24
	v_exp_f32_e32 v25, v25
	v_exp_f32_e32 v30, v30
	v_exp_f32_e32 v31, v31
	v_exp_f32_e32 v28, v28
	v_exp_f32_e32 v29, v29
	v_pk_add_f32 v[26:27], v[26:27], 1.0 op_sel_hi:[1,0]
	v_pk_add_f32 v[24:25], v[24:25], 1.0 op_sel_hi:[1,0]
	v_pk_add_f32 v[30:31], v[30:31], 1.0 op_sel_hi:[1,0]
	v_pk_add_f32 v[28:29], v[28:29], 1.0 op_sel_hi:[1,0]
	v_rcp_f32_e32 v26, v26
	v_rcp_f32_e32 v27, v27
	v_rcp_f32_e32 v24, v24
	v_rcp_f32_e32 v25, v25
	v_rcp_f32_e32 v30, v30
	v_rcp_f32_e32 v31, v31
	v_rcp_f32_e32 v28, v28
	v_rcp_f32_e32 v29, v29
	v_pk_mul_f32 v[20:21], v[20:21], v[26:27]
	v_pk_mul_f32 v[22:23], v[22:23], v[24:25]
	v_pk_mul_f32 v[24:25], v[16:17], v[30:31]
	v_pk_mul_f32 v[16:17], v[18:19], v[28:29]
	v_cvt_pk_f16_f32 v18, v24, v25
	v_cvt_pk_f16_f32 v19, v16, v17
	v_cvt_pk_f16_f32 v17, v22, v23
	v_cvt_pk_f16_f32 v16, v20, v21
	global_store_dwordx4 v[56:57], v[16:19], off offset:256
	v_pk_add_f32 v[6:7], v[6:7], v[14:15]
	v_pk_add_f32 v[4:5], v[4:5], v[12:13]
	v_pk_add_f32 v[2:3], v[2:3], v[10:11]
	v_pk_add_f32 v[0:1], v[0:1], v[8:9]
	v_pk_mul_f32 v[8:9], v[6:7], v[6:7]
	v_pk_mul_f32 v[10:11], v[4:5], v[4:5]
	v_pk_mul_f32 v[12:13], v[2:3], v[2:3]
	v_pk_mul_f32 v[14:15], v[0:1], v[0:1]
	v_pk_fma_f32 v[10:11], v[10:11], s[0:1], v[144:145] op_sel_hi:[1,0,0] neg_lo:[1,0,0] neg_hi:[1,0,0]
	v_pk_fma_f32 v[8:9], v[8:9], s[0:1], v[144:145] op_sel_hi:[1,0,0] neg_lo:[1,0,0] neg_hi:[1,0,0]
	v_pk_fma_f32 v[14:15], v[14:15], s[0:1], v[144:145] op_sel_hi:[1,0,0] neg_lo:[1,0,0] neg_hi:[1,0,0]
	v_pk_fma_f32 v[12:13], v[12:13], s[0:1], v[144:145] op_sel_hi:[1,0,0] neg_lo:[1,0,0] neg_hi:[1,0,0]
	v_pk_mul_f32 v[10:11], v[4:5], v[10:11]
	v_pk_mul_f32 v[8:9], v[6:7], v[8:9]
	v_pk_mul_f32 v[14:15], v[0:1], v[14:15]
	v_pk_mul_f32 v[12:13], v[2:3], v[12:13]
	v_exp_f32_e32 v10, v10
	v_exp_f32_e32 v11, v11
	v_exp_f32_e32 v8, v8
	v_exp_f32_e32 v9, v9
	v_exp_f32_e32 v14, v14
	v_exp_f32_e32 v15, v15
	v_exp_f32_e32 v12, v12
	v_exp_f32_e32 v13, v13
	v_pk_add_f32 v[10:11], v[10:11], 1.0 op_sel_hi:[1,0]
	v_pk_add_f32 v[8:9], v[8:9], 1.0 op_sel_hi:[1,0]
	v_pk_add_f32 v[14:15], v[14:15], 1.0 op_sel_hi:[1,0]
	v_pk_add_f32 v[12:13], v[12:13], 1.0 op_sel_hi:[1,0]
	v_rcp_f32_e32 v10, v10
	v_rcp_f32_e32 v11, v11
	v_rcp_f32_e32 v8, v8
	v_rcp_f32_e32 v9, v9
	v_rcp_f32_e32 v14, v14
	v_rcp_f32_e32 v15, v15
	v_rcp_f32_e32 v12, v12
	v_rcp_f32_e32 v13, v13
	v_pk_mul_f32 v[4:5], v[4:5], v[10:11]
	v_pk_mul_f32 v[6:7], v[6:7], v[8:9]
	v_pk_mul_f32 v[8:9], v[0:1], v[14:15]
	v_pk_mul_f32 v[0:1], v[2:3], v[12:13]
	v_cvt_pk_f16_f32 v2, v8, v9
	v_cvt_pk_f16_f32 v3, v0, v1
	v_cvt_pk_f16_f32 v1, v6, v7
	v_cvt_pk_f16_f32 v0, v4, v5
	global_store_dwordx4 v[40:41], v[0:3], off offset:256
	s_endpgm
	.p2align	8
